# 72 converter workgroups + non-temporal stores for the expert GEMM epilogues (ACT and Y outputs)
# baseline (speedup 1.0000x reference)
; #define LAS __attribute__((address_space(3)))
; __device__ __forceinline__ unsigned pk4_fp8(float a, float b, float c, float d) { int w = 0; w = __builtin_amdgcn_cvt_pk_fp8_f32(a, b, w, false); w = __builtin_amdgcn_cvt_pk_fp8_f32(c, d, w, true); return (unsigned)w; }
;     __device__ __forceinline__ void operator()(const AccT& acc, const pg8::Unit& u, int wr, int wc, int fr, int fq, const LAS float* bl, int nai) const {
;         const int row0 = u.pm * 256 + u.hx * 128 + wr * 64 + fr, a0 = u.pn * 128 + wc * 32 + 8 * fq;
;         unsigned char* act = (unsigned char*)(ws + WS_ACT);
;         const f32x4 bg0 = *(const LAS f32x4*)(bl + 8 * fq), bg1 = *(const LAS f32x4*)(bl + 8 * fq + 4), bu0 = *(const LAS f32x4*)(bl + 32 + 8 * fq), bu1 = *(const LAS f32x4*)(bl + 32 + 8 * fq + 4);
; #pragma unroll
;         for (int ai = 0; ai < 2; ++ai) if (ai < nai)
; #pragma unroll
;             for (int m = 0; m < 4; ++m) { const size_t ro = (size_t)(row0 + ai * 128 + m * 16) * DFF + a0; float o[8];
; #pragma unroll
;                 for (int n = 0; n < 2; ++n) {
;                     f32x4 g4 = acc[ai][0][m][n] + (n ? bg1 : bg0), u4 = acc[ai][1][m][n] + (n ? bu1 : bu0);
; #pragma unroll
;                     for (int j = 0; j < 4; ++j) { g4[j] = fminf(g4[j], 7.0f); u4[j] = __builtin_amdgcn_fmed3f(u4[j], -7.0f, 7.0f); }
;                     const f32x4 t4 = g4 * (-1.702f * 1.4426950408889634f);
;                     f32x4 e4;
; #pragma unroll
;                     for (int j = 0; j < 4; ++j) e4[j] = __builtin_amdgcn_exp2f(t4[j]);
;                     e4 = e4 + 1.0f;
;                     f32x4 r4;
; #pragma unroll
;                     for (int j = 0; j < 4; ++j) r4[j] = __builtin_amdgcn_rcpf(e4[j]);
;                     const f32x4 o4 = (u4 * A8_SCALE + A8_SCALE) * (g4 * r4);
; #pragma unroll
;                     for (int j = 0; j < 4; ++j) o[4 * n + j] = o4[j]; }
;                 u32x2 w; w.x = pk4_fp8(o[0], o[1], o[2], o[3]); w.y = pk4_fp8(o[4], o[5], o[6], o[7]);
;                 *(u32x2*)(act + ro) = w; }
.LBB0_1142:
	s_nop 15
	s_nop 15
	ds_read_b128 v[14:17], v220
	ds_read_b128 v[6:9], v220 offset:16
	ds_read_b128 v[10:13], v220 offset:128
	ds_read_b128 v[2:5], v220 offset:144
	v_lshl_or_b32 v18, s46, 7, v222
	s_waitcnt lgkmcnt(3)
	v_pk_add_f32 v[22:23], v[172:173], v[16:17]
	v_pk_add_f32 v[24:25], v[170:171], v[14:15]
	v_min_f32_e32 v22, 0x40e00000, v22
	v_min_f32_e32 v24, 0x40e00000, v24
	v_min_f32_e32 v25, 0x40e00000, v25
	v_min_f32_e32 v23, 0x40e00000, v23
	v_mul_f32_e32 v21, 0xc01d265f, v24
	v_mul_f32_e32 v31, 0xc01d265f, v22
	v_exp_f32_e32 v30, v21
	v_mul_f32_e32 v21, 0xc01d265f, v25
	v_exp_f32_e32 v32, v31
	v_mul_f32_e32 v31, 0xc01d265f, v23
	v_exp_f32_e32 v33, v31
	v_exp_f32_e32 v31, v21
	s_waitcnt lgkmcnt(1)
	v_pk_add_f32 v[28:29], v[178:179], v[10:11]
	v_pk_add_f32 v[26:27], v[180:181], v[12:13]
	v_med3_f32 v21, v28, s80, v225
	v_pk_add_f32 v[30:31], v[30:31], 1.0 op_sel_hi:[1,0]
	v_med3_f32 v34, v29, s80, v225
	v_rcp_f32_e32 v30, v30
	v_rcp_f32_e32 v31, v31
	v_pk_add_f32 v[28:29], v[32:33], 1.0 op_sel_hi:[1,0]
	v_fma_f32 v21, v21, 4.0, 4.0
	v_rcp_f32_e32 v28, v28
	v_rcp_f32_e32 v29, v29
	v_pk_mul_f32 v[24:25], v[24:25], v[30:31]
	v_med3_f32 v26, v26, s80, v225
	v_mul_f32_e32 v21, v21, v24
	v_fma_f32 v24, v34, 4.0, 4.0
	v_med3_f32 v27, v27, s80, v225
	v_pk_mul_f32 v[22:23], v[22:23], v[28:29]
	v_mul_f32_e32 v34, v24, v25
	v_fma_f32 v24, v26, 4.0, 4.0
	v_mul_f32_e32 v35, v24, v22
	v_fma_f32 v22, v27, 4.0, 4.0
	v_mul_f32_e32 v36, v22, v23
	v_pk_add_f32 v[22:23], v[168:169], v[8:9]
	v_pk_add_f32 v[24:25], v[166:167], v[6:7]
	v_min_f32_e32 v22, 0x40e00000, v22
	v_min_f32_e32 v24, 0x40e00000, v24
	v_min_f32_e32 v25, 0x40e00000, v25
	v_min_f32_e32 v23, 0x40e00000, v23
	v_mul_f32_e32 v30, 0xc01d265f, v24
	v_mul_f32_e32 v31, 0xc01d265f, v25
	v_mul_f32_e32 v32, 0xc01d265f, v22
	v_mul_f32_e32 v33, 0xc01d265f, v23
	v_exp_f32_e32 v30, v30
	v_exp_f32_e32 v32, v32
	v_exp_f32_e32 v33, v33
	v_exp_f32_e32 v31, v31
	s_waitcnt lgkmcnt(0)
	v_pk_add_f32 v[28:29], v[174:175], v[2:3]
	v_pk_add_f32 v[26:27], v[176:177], v[4:5]
	v_med3_f32 v37, v28, s80, v225
	v_med3_f32 v38, v29, s80, v225
	v_pk_add_f32 v[28:29], v[32:33], 1.0 op_sel_hi:[1,0]
	v_pk_add_f32 v[30:31], v[30:31], 1.0 op_sel_hi:[1,0]
	v_rcp_f32_e32 v28, v28
	v_rcp_f32_e32 v30, v30
	v_rcp_f32_e32 v29, v29
	v_rcp_f32_e32 v31, v31
	v_med3_f32 v26, v26, s80, v225
	v_med3_f32 v27, v27, s80, v225
	v_pk_mul_f32 v[22:23], v[22:23], v[28:29]
	v_pk_mul_f32 v[24:25], v[24:25], v[30:31]
	v_fma_f32 v28, v37, 4.0, 4.0
	v_mul_f32_e32 v28, v28, v24
	v_fma_f32 v24, v38, 4.0, 4.0
	v_mul_f32_e32 v29, v24, v25
	v_fma_f32 v24, v26, 4.0, 4.0
	v_mul_f32_e32 v22, v24, v22
	v_mov_b32_e32 v24, 0
	v_mov_b32_e32 v25, 0
	v_cvt_pk_fp8_f32 v24, v21, v34
	v_cvt_pk_fp8_f32 v25, v28, v29
	v_fma_f32 v21, v27, 4.0, 4.0
	v_mul_f32_e32 v21, v21, v23
	v_lshl_add_u32 v20, s84, 8, v219
	v_cvt_pk_fp8_f32 v24, v35, v36 op_sel:[0,0,1]
	v_cvt_pk_fp8_f32 v25, v22, v21 op_sel:[0,0,1]
	v_ashrrev_i32_e32 v19, 31, v18
	v_ashrrev_i32_e32 v21, 31, v20
	v_lshl_add_u64 v[18:19], s[28:29], 0, v[18:19]
	v_lshlrev_b64 v[22:23], 11, v[20:21]
	v_lshl_add_u64 v[22:23], v[18:19], 0, v[22:23]
	v_pk_add_f32 v[26:27], v[154:155], v[14:15]
	global_store_dwordx2 v[22:23], v[24:25], off nt
	v_pk_add_f32 v[24:25], v[156:157], v[16:17]
	v_min_f32_e32 v26, 0x40e00000, v26
	v_min_f32_e32 v27, 0x40e00000, v27
	v_min_f32_e32 v24, 0x40e00000, v24
	v_mul_f32_e32 v21, 0xc01d265f, v26
	v_min_f32_e32 v25, 0x40e00000, v25
	v_exp_f32_e32 v32, v21
	v_mul_f32_e32 v21, 0xc01d265f, v27
	v_mul_f32_e32 v23, 0xc01d265f, v24
	v_exp_f32_e32 v34, v23
	v_mul_f32_e32 v23, 0xc01d265f, v25
	v_exp_f32_e32 v33, v21
	v_exp_f32_e32 v35, v23
	v_pk_add_f32 v[30:31], v[162:163], v[10:11]
	v_pk_add_f32 v[28:29], v[164:165], v[12:13]
	v_pk_add_f32 v[32:33], v[32:33], 1.0 op_sel_hi:[1,0]
	v_med3_f32 v21, v30, s80, v225
	v_med3_f32 v23, v31, s80, v225
	v_pk_add_f32 v[30:31], v[34:35], 1.0 op_sel_hi:[1,0]
	v_rcp_f32_e32 v32, v32
	v_rcp_f32_e32 v33, v33
	v_rcp_f32_e32 v30, v30
	v_rcp_f32_e32 v31, v31
	v_med3_f32 v28, v28, s80, v225
	v_pk_mul_f32 v[26:27], v[26:27], v[32:33]
	v_fma_f32 v21, v21, 4.0, 4.0
	v_med3_f32 v29, v29, s80, v225
	v_pk_mul_f32 v[24:25], v[24:25], v[30:31]
	v_mul_f32_e32 v21, v21, v26
	v_fma_f32 v26, v28, 4.0, 4.0
	v_fma_f32 v23, v23, 4.0, 4.0
	v_mul_f32_e32 v36, v26, v24
	v_fma_f32 v24, v29, 4.0, 4.0
	v_mul_f32_e32 v23, v23, v27
	v_mul_f32_e32 v37, v24, v25
	v_pk_add_f32 v[24:25], v[152:153], v[8:9]
	v_pk_add_f32 v[26:27], v[150:151], v[6:7]
	v_min_f32_e32 v24, 0x40e00000, v24
	v_min_f32_e32 v26, 0x40e00000, v26
	v_min_f32_e32 v27, 0x40e00000, v27
	v_min_f32_e32 v25, 0x40e00000, v25
	v_mul_f32_e32 v32, 0xc01d265f, v26
	v_mul_f32_e32 v33, 0xc01d265f, v27
	v_mul_f32_e32 v34, 0xc01d265f, v24
	v_mul_f32_e32 v35, 0xc01d265f, v25
	v_exp_f32_e32 v32, v32
	v_exp_f32_e32 v34, v34
	v_exp_f32_e32 v35, v35
	v_exp_f32_e32 v33, v33
	v_pk_add_f32 v[30:31], v[158:159], v[2:3]
	v_pk_add_f32 v[28:29], v[160:161], v[4:5]
	v_med3_f32 v38, v30, s80, v225
	v_med3_f32 v39, v31, s80, v225
	v_pk_add_f32 v[30:31], v[34:35], 1.0 op_sel_hi:[1,0]
	v_pk_add_f32 v[32:33], v[32:33], 1.0 op_sel_hi:[1,0]
	v_rcp_f32_e32 v30, v30
	v_rcp_f32_e32 v32, v32
	v_rcp_f32_e32 v31, v31
	v_rcp_f32_e32 v33, v33
	v_med3_f32 v28, v28, s80, v225
	v_med3_f32 v29, v29, s80, v225
	v_pk_mul_f32 v[24:25], v[24:25], v[30:31]
	v_pk_mul_f32 v[26:27], v[26:27], v[32:33]
	v_fma_f32 v30, v38, 4.0, 4.0
	v_mul_f32_e32 v30, v30, v26
	v_fma_f32 v26, v39, 4.0, 4.0
	v_mul_f32_e32 v31, v26, v27
	v_fma_f32 v26, v28, 4.0, 4.0
	v_mul_f32_e32 v24, v26, v24
	v_mov_b32_e32 v26, 0
	v_mov_b32_e32 v27, 0
	v_cvt_pk_fp8_f32 v26, v21, v23
; #define LAS __attribute__((address_space(3)))
; __device__ __forceinline__ unsigned pk4_fp8(float a, float b, float c, float d) { int w = 0; w = __builtin_amdgcn_cvt_pk_fp8_f32(a, b, w, false); w = __builtin_amdgcn_cvt_pk_fp8_f32(c, d, w, true); return (unsigned)w; }
;     __device__ __forceinline__ void operator()(const AccT& acc, const pg8::Unit& u, int wr, int wc, int fr, int fq, const LAS float* bl, int nai) const {
;         const int row0 = u.pm * 256 + u.hx * 128 + wr * 64 + fr, a0 = u.pn * 128 + wc * 32 + 8 * fq;
;         unsigned char* act = (unsigned char*)(ws + WS_ACT);
;         const f32x4 bg0 = *(const LAS f32x4*)(bl + 8 * fq), bg1 = *(const LAS f32x4*)(bl + 8 * fq + 4), bu0 = *(const LAS f32x4*)(bl + 32 + 8 * fq), bu1 = *(const LAS f32x4*)(bl + 32 + 8 * fq + 4);
; #pragma unroll
;         for (int ai = 0; ai < 2; ++ai) if (ai < nai)
; #pragma unroll
;             for (int m = 0; m < 4; ++m) { const size_t ro = (size_t)(row0 + ai * 128 + m * 16) * DFF + a0; float o[8];
; #pragma unroll
;                 for (int n = 0; n < 2; ++n) {
;                     f32x4 g4 = acc[ai][0][m][n] + (n ? bg1 : bg0), u4 = acc[ai][1][m][n] + (n ? bu1 : bu0);
; #pragma unroll
;                     for (int j = 0; j < 4; ++j) { g4[j] = fminf(g4[j], 7.0f); u4[j] = __builtin_amdgcn_fmed3f(u4[j], -7.0f, 7.0f); }
;                     const f32x4 t4 = g4 * (-1.702f * 1.4426950408889634f);
;                     f32x4 e4;
; #pragma unroll
;                     for (int j = 0; j < 4; ++j) e4[j] = __builtin_amdgcn_exp2f(t4[j]);
;                     e4 = e4 + 1.0f;
;                     f32x4 r4;
; #pragma unroll
;                     for (int j = 0; j < 4; ++j) r4[j] = __builtin_amdgcn_rcpf(e4[j]);
;                     const f32x4 o4 = (u4 * A8_SCALE + A8_SCALE) * (g4 * r4);
; #pragma unroll
;                     for (int j = 0; j < 4; ++j) o[4 * n + j] = o4[j]; }
;                 u32x2 w; w.x = pk4_fp8(o[0], o[1], o[2], o[3]); w.y = pk4_fp8(o[4], o[5], o[6], o[7]);
;                 *(u32x2*)(act + ro) = w; }
	v_cvt_pk_fp8_f32 v27, v30, v31
	v_fma_f32 v21, v29, 4.0, 4.0
	v_mul_f32_e32 v21, v21, v25
	v_or_b32_e32 v22, 16, v20
	v_cvt_pk_fp8_f32 v26, v36, v37 op_sel:[0,0,1]
	v_cvt_pk_fp8_f32 v27, v24, v21 op_sel:[0,0,1]
	v_ashrrev_i32_e32 v23, 31, v22
	v_lshlrev_b64 v[22:23], 11, v[22:23]
	v_lshl_add_u64 v[22:23], v[18:19], 0, v[22:23]
	global_store_dwordx2 v[22:23], v[26:27], off nt
	v_pk_add_f32 v[26:27], v[142:143], v[14:15]
	v_pk_add_f32 v[24:25], v[144:145], v[16:17]
	v_min_f32_e32 v26, 0x40e00000, v26
	v_min_f32_e32 v27, 0x40e00000, v27
	v_min_f32_e32 v24, 0x40e00000, v24
	v_mul_f32_e32 v21, 0xc01d265f, v26
	v_min_f32_e32 v25, 0x40e00000, v25
	v_exp_f32_e32 v32, v21
	v_mul_f32_e32 v21, 0xc01d265f, v27
	v_mul_f32_e32 v23, 0xc01d265f, v24
	v_exp_f32_e32 v34, v23
	v_mul_f32_e32 v23, 0xc01d265f, v25
	v_exp_f32_e32 v33, v21
	v_exp_f32_e32 v35, v23
	v_pk_add_f32 v[30:31], v[146:147], v[10:11]
	v_pk_add_f32 v[28:29], v[148:149], v[12:13]
	v_pk_add_f32 v[32:33], v[32:33], 1.0 op_sel_hi:[1,0]
	v_med3_f32 v21, v30, s80, v225
	v_med3_f32 v23, v31, s80, v225
	v_pk_add_f32 v[30:31], v[34:35], 1.0 op_sel_hi:[1,0]
	v_rcp_f32_e32 v32, v32
	v_rcp_f32_e32 v33, v33
	v_rcp_f32_e32 v30, v30
	v_rcp_f32_e32 v31, v31
	v_med3_f32 v28, v28, s80, v225
	v_pk_mul_f32 v[26:27], v[26:27], v[32:33]
	v_fma_f32 v21, v21, 4.0, 4.0
	v_med3_f32 v29, v29, s80, v225
	v_pk_mul_f32 v[24:25], v[24:25], v[30:31]
	v_mul_f32_e32 v21, v21, v26
	v_fma_f32 v26, v28, 4.0, 4.0
	v_fma_f32 v23, v23, 4.0, 4.0
	v_mul_f32_e32 v36, v26, v24
	v_fma_f32 v24, v29, 4.0, 4.0
	v_mul_f32_e32 v23, v23, v27
	v_mul_f32_e32 v37, v24, v25
	v_pk_add_f32 v[24:25], v[136:137], v[8:9]
	v_pk_add_f32 v[26:27], v[134:135], v[6:7]
	v_min_f32_e32 v24, 0x40e00000, v24
	v_min_f32_e32 v26, 0x40e00000, v26
	v_min_f32_e32 v27, 0x40e00000, v27
	v_min_f32_e32 v25, 0x40e00000, v25
	v_mul_f32_e32 v32, 0xc01d265f, v26
	v_mul_f32_e32 v33, 0xc01d265f, v27
	v_mul_f32_e32 v34, 0xc01d265f, v24
	v_mul_f32_e32 v35, 0xc01d265f, v25
	v_exp_f32_e32 v32, v32
	v_exp_f32_e32 v34, v34
	v_exp_f32_e32 v35, v35
	v_exp_f32_e32 v33, v33
	v_pk_add_f32 v[30:31], v[138:139], v[2:3]
	v_pk_add_f32 v[28:29], v[140:141], v[4:5]
	v_med3_f32 v38, v30, s80, v225
	v_med3_f32 v39, v31, s80, v225
	v_pk_add_f32 v[30:31], v[34:35], 1.0 op_sel_hi:[1,0]
	v_pk_add_f32 v[32:33], v[32:33], 1.0 op_sel_hi:[1,0]
	v_rcp_f32_e32 v30, v30
	v_rcp_f32_e32 v32, v32
	v_rcp_f32_e32 v31, v31
	v_rcp_f32_e32 v33, v33
	v_med3_f32 v28, v28, s80, v225
	v_med3_f32 v29, v29, s80, v225
	v_pk_mul_f32 v[24:25], v[24:25], v[30:31]
	v_pk_mul_f32 v[26:27], v[26:27], v[32:33]
	v_fma_f32 v30, v38, 4.0, 4.0
	v_mul_f32_e32 v30, v30, v26
	v_fma_f32 v26, v39, 4.0, 4.0
	v_mul_f32_e32 v31, v26, v27
	v_fma_f32 v26, v28, 4.0, 4.0
	v_mul_f32_e32 v24, v26, v24
	v_mov_b32_e32 v26, 0
	v_mov_b32_e32 v27, 0
	v_cvt_pk_fp8_f32 v26, v21, v23
	v_cvt_pk_fp8_f32 v27, v30, v31
	v_fma_f32 v21, v29, 4.0, 4.0
	v_mul_f32_e32 v21, v21, v25
	v_or_b32_e32 v22, 32, v20
	v_cvt_pk_fp8_f32 v26, v36, v37 op_sel:[0,0,1]
	v_cvt_pk_fp8_f32 v27, v24, v21 op_sel:[0,0,1]
	v_ashrrev_i32_e32 v23, 31, v22
	v_lshlrev_b64 v[22:23], 11, v[22:23]
	v_lshl_add_u64 v[22:23], v[18:19], 0, v[22:23]
	global_store_dwordx2 v[22:23], v[26:27], off nt
	v_pk_add_f32 v[26:27], v[118:119], v[14:15]
	v_pk_add_f32 v[24:25], v[120:121], v[16:17]
	v_min_f32_e32 v26, 0x40e00000, v26
	v_min_f32_e32 v27, 0x40e00000, v27
	v_min_f32_e32 v24, 0x40e00000, v24
	v_mul_f32_e32 v21, 0xc01d265f, v26
	v_min_f32_e32 v25, 0x40e00000, v25
	v_exp_f32_e32 v32, v21
	v_mul_f32_e32 v21, 0xc01d265f, v27
	v_mul_f32_e32 v23, 0xc01d265f, v24
	v_exp_f32_e32 v34, v23
	v_mul_f32_e32 v23, 0xc01d265f, v25
	v_exp_f32_e32 v33, v21
	v_exp_f32_e32 v35, v23
	v_pk_add_f32 v[30:31], v[126:127], v[10:11]
	v_pk_add_f32 v[28:29], v[128:129], v[12:13]
	v_pk_add_f32 v[32:33], v[32:33], 1.0 op_sel_hi:[1,0]
	v_med3_f32 v21, v30, s80, v225
	v_med3_f32 v23, v31, s80, v225
	v_pk_add_f32 v[30:31], v[34:35], 1.0 op_sel_hi:[1,0]
	v_rcp_f32_e32 v32, v32
	v_rcp_f32_e32 v33, v33
	v_rcp_f32_e32 v30, v30
	v_rcp_f32_e32 v31, v31
	v_med3_f32 v28, v28, s80, v225
	v_pk_mul_f32 v[26:27], v[26:27], v[32:33]
	v_fma_f32 v21, v21, 4.0, 4.0
	v_med3_f32 v29, v29, s80, v225
	v_pk_mul_f32 v[24:25], v[24:25], v[30:31]
	v_mul_f32_e32 v21, v21, v26
	v_fma_f32 v26, v28, 4.0, 4.0
	v_fma_f32 v23, v23, 4.0, 4.0
	v_mul_f32_e32 v36, v26, v24
	v_fma_f32 v24, v29, 4.0, 4.0
	v_mul_f32_e32 v23, v23, v27
	v_mul_f32_e32 v37, v24, v25
	v_pk_add_f32 v[24:25], v[112:113], v[8:9]
	v_pk_add_f32 v[26:27], v[110:111], v[6:7]
	v_min_f32_e32 v24, 0x40e00000, v24
	v_min_f32_e32 v26, 0x40e00000, v26
	v_min_f32_e32 v27, 0x40e00000, v27
	v_min_f32_e32 v25, 0x40e00000, v25
	v_mul_f32_e32 v32, 0xc01d265f, v26
	v_mul_f32_e32 v33, 0xc01d265f, v27
	v_mul_f32_e32 v34, 0xc01d265f, v24
	v_mul_f32_e32 v35, 0xc01d265f, v25
	v_exp_f32_e32 v32, v32
	v_exp_f32_e32 v34, v34
	v_exp_f32_e32 v35, v35
	v_exp_f32_e32 v33, v33
	v_pk_add_f32 v[30:31], v[98:99], v[2:3]
	v_pk_add_f32 v[28:29], v[100:101], v[4:5]
	v_med3_f32 v38, v30, s80, v225
	v_med3_f32 v39, v31, s80, v225
	v_pk_add_f32 v[30:31], v[34:35], 1.0 op_sel_hi:[1,0]
	v_pk_add_f32 v[32:33], v[32:33], 1.0 op_sel_hi:[1,0]
	v_rcp_f32_e32 v30, v30
	v_rcp_f32_e32 v32, v32
	v_rcp_f32_e32 v31, v31
	v_rcp_f32_e32 v33, v33
	v_med3_f32 v28, v28, s80, v225
	v_med3_f32 v29, v29, s80, v225
	v_pk_mul_f32 v[24:25], v[24:25], v[30:31]
	v_pk_mul_f32 v[26:27], v[26:27], v[32:33]
	v_fma_f32 v30, v38, 4.0, 4.0
	v_mul_f32_e32 v30, v30, v26
	v_fma_f32 v26, v39, 4.0, 4.0
	v_mul_f32_e32 v31, v26, v27
	v_fma_f32 v26, v28, 4.0, 4.0
	v_mul_f32_e32 v24, v26, v24
	v_mov_b32_e32 v26, 0
	v_mov_b32_e32 v27, 0
	v_cvt_pk_fp8_f32 v26, v21, v23
; #define LAS __attribute__((address_space(3)))
; __device__ __forceinline__ unsigned pk4_fp8(float a, float b, float c, float d) { int w = 0; w = __builtin_amdgcn_cvt_pk_fp8_f32(a, b, w, false); w = __builtin_amdgcn_cvt_pk_fp8_f32(c, d, w, true); return (unsigned)w; }
;     __device__ __forceinline__ void operator()(const AccT& acc, const pg8::Unit& u, int wr, int wc, int fr, int fq, const LAS float* bl, int nai) const {
;         const int row0 = u.pm * 256 + u.hx * 128 + wr * 64 + fr, a0 = u.pn * 128 + wc * 32 + 8 * fq;
;         unsigned char* act = (unsigned char*)(ws + WS_ACT);
;         const f32x4 bg0 = *(const LAS f32x4*)(bl + 8 * fq), bg1 = *(const LAS f32x4*)(bl + 8 * fq + 4), bu0 = *(const LAS f32x4*)(bl + 32 + 8 * fq), bu1 = *(const LAS f32x4*)(bl + 32 + 8 * fq + 4);
; #pragma unroll
;         for (int ai = 0; ai < 2; ++ai) if (ai < nai)
; #pragma unroll
;             for (int m = 0; m < 4; ++m) { const size_t ro = (size_t)(row0 + ai * 128 + m * 16) * DFF + a0; float o[8];
; #pragma unroll
;                 for (int n = 0; n < 2; ++n) {
;                     f32x4 g4 = acc[ai][0][m][n] + (n ? bg1 : bg0), u4 = acc[ai][1][m][n] + (n ? bu1 : bu0);
; #pragma unroll
;                     for (int j = 0; j < 4; ++j) { g4[j] = fminf(g4[j], 7.0f); u4[j] = __builtin_amdgcn_fmed3f(u4[j], -7.0f, 7.0f); }
;                     const f32x4 t4 = g4 * (-1.702f * 1.4426950408889634f);
;                     f32x4 e4;
; #pragma unroll
;                     for (int j = 0; j < 4; ++j) e4[j] = __builtin_amdgcn_exp2f(t4[j]);
;                     e4 = e4 + 1.0f;
;                     f32x4 r4;
; #pragma unroll
;                     for (int j = 0; j < 4; ++j) r4[j] = __builtin_amdgcn_rcpf(e4[j]);
;                     const f32x4 o4 = (u4 * A8_SCALE + A8_SCALE) * (g4 * r4);
; #pragma unroll
;                     for (int j = 0; j < 4; ++j) o[4 * n + j] = o4[j]; }
;                 u32x2 w; w.x = pk4_fp8(o[0], o[1], o[2], o[3]); w.y = pk4_fp8(o[4], o[5], o[6], o[7]);
;                 *(u32x2*)(act + ro) = w; }
	v_cvt_pk_fp8_f32 v27, v30, v31
	v_fma_f32 v21, v29, 4.0, 4.0
	v_mul_f32_e32 v21, v21, v25
	v_or_b32_e32 v22, 48, v20
	v_cvt_pk_fp8_f32 v26, v36, v37 op_sel:[0,0,1]
	v_cvt_pk_fp8_f32 v27, v24, v21 op_sel:[0,0,1]
	v_ashrrev_i32_e32 v23, 31, v22
	v_lshlrev_b64 v[22:23], 11, v[22:23]
	v_lshl_add_u64 v[22:23], v[18:19], 0, v[22:23]
	global_store_dwordx2 v[22:23], v[26:27], off nt
	v_pk_add_f32 v[26:27], v[114:115], v[14:15]
	v_pk_add_f32 v[24:25], v[116:117], v[16:17]
	v_min_f32_e32 v26, 0x40e00000, v26
	v_min_f32_e32 v27, 0x40e00000, v27
	v_min_f32_e32 v24, 0x40e00000, v24
	v_mul_f32_e32 v21, 0xc01d265f, v26
	v_min_f32_e32 v25, 0x40e00000, v25
	v_exp_f32_e32 v32, v21
	v_mul_f32_e32 v21, 0xc01d265f, v27
	v_mul_f32_e32 v23, 0xc01d265f, v24
	v_exp_f32_e32 v34, v23
	v_mul_f32_e32 v23, 0xc01d265f, v25
	v_exp_f32_e32 v33, v21
	v_exp_f32_e32 v35, v23
	v_pk_add_f32 v[30:31], v[130:131], v[10:11]
	v_pk_add_f32 v[28:29], v[132:133], v[12:13]
	v_pk_add_f32 v[32:33], v[32:33], 1.0 op_sel_hi:[1,0]
	v_med3_f32 v21, v30, s80, v225
	v_med3_f32 v23, v31, s80, v225
	v_pk_add_f32 v[30:31], v[34:35], 1.0 op_sel_hi:[1,0]
	v_rcp_f32_e32 v32, v32
	v_rcp_f32_e32 v33, v33
	v_rcp_f32_e32 v30, v30
	v_rcp_f32_e32 v31, v31
	v_med3_f32 v28, v28, s80, v225
	v_pk_mul_f32 v[26:27], v[26:27], v[32:33]
	v_fma_f32 v21, v21, 4.0, 4.0
	v_med3_f32 v29, v29, s80, v225
	v_pk_mul_f32 v[24:25], v[24:25], v[30:31]
	v_mul_f32_e32 v21, v21, v26
	v_fma_f32 v26, v28, 4.0, 4.0
	v_fma_f32 v23, v23, 4.0, 4.0
	v_mul_f32_e32 v36, v26, v24
	v_fma_f32 v24, v29, 4.0, 4.0
	v_mul_f32_e32 v23, v23, v27
	v_mul_f32_e32 v37, v24, v25
	v_pk_add_f32 v[24:25], v[108:109], v[8:9]
	v_pk_add_f32 v[26:27], v[106:107], v[6:7]
	v_min_f32_e32 v24, 0x40e00000, v24
	v_min_f32_e32 v26, 0x40e00000, v26
	v_min_f32_e32 v27, 0x40e00000, v27
	v_min_f32_e32 v25, 0x40e00000, v25
	v_mul_f32_e32 v32, 0xc01d265f, v26
	v_mul_f32_e32 v33, 0xc01d265f, v27
	v_mul_f32_e32 v34, 0xc01d265f, v24
	v_mul_f32_e32 v35, 0xc01d265f, v25
	v_exp_f32_e32 v32, v32
	v_exp_f32_e32 v34, v34
	v_exp_f32_e32 v35, v35
	v_exp_f32_e32 v33, v33
	v_pk_add_f32 v[30:31], v[122:123], v[2:3]
	v_pk_add_f32 v[28:29], v[124:125], v[4:5]
	v_med3_f32 v38, v30, s80, v225
	v_med3_f32 v39, v31, s80, v225
	v_pk_add_f32 v[30:31], v[34:35], 1.0 op_sel_hi:[1,0]
	v_pk_add_f32 v[32:33], v[32:33], 1.0 op_sel_hi:[1,0]
	v_rcp_f32_e32 v30, v30
	v_rcp_f32_e32 v32, v32
	v_rcp_f32_e32 v31, v31
	v_rcp_f32_e32 v33, v33
	v_med3_f32 v28, v28, s80, v225
	v_med3_f32 v29, v29, s80, v225
	v_pk_mul_f32 v[24:25], v[24:25], v[30:31]
	v_pk_mul_f32 v[26:27], v[26:27], v[32:33]
	v_fma_f32 v30, v38, 4.0, 4.0
	v_mul_f32_e32 v30, v30, v26
	v_fma_f32 v26, v39, 4.0, 4.0
	v_mul_f32_e32 v31, v26, v27
	v_fma_f32 v26, v28, 4.0, 4.0
	v_mul_f32_e32 v24, v26, v24
	v_mov_b32_e32 v26, 0
	v_mov_b32_e32 v27, 0
	v_cvt_pk_fp8_f32 v26, v21, v23
	v_cvt_pk_fp8_f32 v27, v30, v31
	v_fma_f32 v21, v29, 4.0, 4.0
	v_mul_f32_e32 v21, v21, v25
	v_add_u32_e32 v22, 0x80, v20
	v_cvt_pk_fp8_f32 v26, v36, v37 op_sel:[0,0,1]
	v_cvt_pk_fp8_f32 v27, v24, v21 op_sel:[0,0,1]
	v_ashrrev_i32_e32 v23, 31, v22
	v_lshlrev_b64 v[22:23], 11, v[22:23]
	v_lshl_add_u64 v[22:23], v[18:19], 0, v[22:23]
	global_store_dwordx2 v[22:23], v[26:27], off nt
	v_pk_add_f32 v[26:27], v[94:95], v[14:15]
	v_pk_add_f32 v[24:25], v[96:97], v[16:17]
	v_min_f32_e32 v26, 0x40e00000, v26
	v_min_f32_e32 v27, 0x40e00000, v27
	v_min_f32_e32 v24, 0x40e00000, v24
	v_mul_f32_e32 v21, 0xc01d265f, v26
	v_min_f32_e32 v25, 0x40e00000, v25
	v_exp_f32_e32 v32, v21
	v_mul_f32_e32 v21, 0xc01d265f, v27
	v_mul_f32_e32 v23, 0xc01d265f, v24
	v_exp_f32_e32 v34, v23
	v_mul_f32_e32 v23, 0xc01d265f, v25
	v_exp_f32_e32 v33, v21
	v_exp_f32_e32 v35, v23
	v_pk_add_f32 v[30:31], v[102:103], v[10:11]
	v_pk_add_f32 v[28:29], v[104:105], v[12:13]
	v_pk_add_f32 v[32:33], v[32:33], 1.0 op_sel_hi:[1,0]
	v_med3_f32 v21, v30, s80, v225
	v_med3_f32 v23, v31, s80, v225
	v_pk_add_f32 v[30:31], v[34:35], 1.0 op_sel_hi:[1,0]
	v_rcp_f32_e32 v32, v32
	v_rcp_f32_e32 v33, v33
	v_rcp_f32_e32 v30, v30
	v_rcp_f32_e32 v31, v31
	v_med3_f32 v28, v28, s80, v225
	v_pk_mul_f32 v[26:27], v[26:27], v[32:33]
	v_fma_f32 v21, v21, 4.0, 4.0
	v_med3_f32 v29, v29, s80, v225
	v_pk_mul_f32 v[24:25], v[24:25], v[30:31]
	v_mul_f32_e32 v21, v21, v26
	v_fma_f32 v26, v28, 4.0, 4.0
	v_fma_f32 v23, v23, 4.0, 4.0
	v_mul_f32_e32 v36, v26, v24
	v_fma_f32 v24, v29, 4.0, 4.0
	v_mul_f32_e32 v23, v23, v27
	v_mul_f32_e32 v37, v24, v25
	v_pk_add_f32 v[24:25], v[88:89], v[8:9]
	v_pk_add_f32 v[26:27], v[86:87], v[6:7]
	v_min_f32_e32 v24, 0x40e00000, v24
	v_min_f32_e32 v26, 0x40e00000, v26
	v_min_f32_e32 v27, 0x40e00000, v27
	v_min_f32_e32 v25, 0x40e00000, v25
	v_mul_f32_e32 v32, 0xc01d265f, v26
	v_mul_f32_e32 v33, 0xc01d265f, v27
	v_mul_f32_e32 v34, 0xc01d265f, v24
	v_mul_f32_e32 v35, 0xc01d265f, v25
	v_exp_f32_e32 v32, v32
	v_exp_f32_e32 v34, v34
	v_exp_f32_e32 v35, v35
	v_exp_f32_e32 v33, v33
	v_pk_add_f32 v[30:31], v[90:91], v[2:3]
	v_pk_add_f32 v[28:29], v[92:93], v[4:5]
	v_med3_f32 v38, v30, s80, v225
	v_med3_f32 v39, v31, s80, v225
	v_pk_add_f32 v[30:31], v[34:35], 1.0 op_sel_hi:[1,0]
	v_pk_add_f32 v[32:33], v[32:33], 1.0 op_sel_hi:[1,0]
	v_rcp_f32_e32 v30, v30
	v_rcp_f32_e32 v32, v32
	v_rcp_f32_e32 v31, v31
	v_rcp_f32_e32 v33, v33
	v_med3_f32 v28, v28, s80, v225
	v_med3_f32 v29, v29, s80, v225
	v_pk_mul_f32 v[24:25], v[24:25], v[30:31]
	v_pk_mul_f32 v[26:27], v[26:27], v[32:33]
	v_fma_f32 v30, v38, 4.0, 4.0
	v_mul_f32_e32 v30, v30, v26
	v_fma_f32 v26, v39, 4.0, 4.0
	v_mul_f32_e32 v31, v26, v27
	v_fma_f32 v26, v28, 4.0, 4.0
	v_mul_f32_e32 v24, v26, v24
	v_mov_b32_e32 v26, 0
	v_mov_b32_e32 v27, 0
	v_cvt_pk_fp8_f32 v26, v21, v23
; #define LAS __attribute__((address_space(3)))
; __device__ __forceinline__ unsigned pk4_fp8(float a, float b, float c, float d) { int w = 0; w = __builtin_amdgcn_cvt_pk_fp8_f32(a, b, w, false); w = __builtin_amdgcn_cvt_pk_fp8_f32(c, d, w, true); return (unsigned)w; }
;     __device__ __forceinline__ void operator()(const AccT& acc, const pg8::Unit& u, int wr, int wc, int fr, int fq, const LAS float* bl, int nai) const {
;         const int row0 = u.pm * 256 + u.hx * 128 + wr * 64 + fr, a0 = u.pn * 128 + wc * 32 + 8 * fq;
;         unsigned char* act = (unsigned char*)(ws + WS_ACT);
;         const f32x4 bg0 = *(const LAS f32x4*)(bl + 8 * fq), bg1 = *(const LAS f32x4*)(bl + 8 * fq + 4), bu0 = *(const LAS f32x4*)(bl + 32 + 8 * fq), bu1 = *(const LAS f32x4*)(bl + 32 + 8 * fq + 4);
; #pragma unroll
;         for (int ai = 0; ai < 2; ++ai) if (ai < nai)
; #pragma unroll
;             for (int m = 0; m < 4; ++m) { const size_t ro = (size_t)(row0 + ai * 128 + m * 16) * DFF + a0; float o[8];
; #pragma unroll
;                 for (int n = 0; n < 2; ++n) {
;                     f32x4 g4 = acc[ai][0][m][n] + (n ? bg1 : bg0), u4 = acc[ai][1][m][n] + (n ? bu1 : bu0);
; #pragma unroll
;                     for (int j = 0; j < 4; ++j) { g4[j] = fminf(g4[j], 7.0f); u4[j] = __builtin_amdgcn_fmed3f(u4[j], -7.0f, 7.0f); }
;                     const f32x4 t4 = g4 * (-1.702f * 1.4426950408889634f);
;                     f32x4 e4;
; #pragma unroll
;                     for (int j = 0; j < 4; ++j) e4[j] = __builtin_amdgcn_exp2f(t4[j]);
;                     e4 = e4 + 1.0f;
;                     f32x4 r4;
; #pragma unroll
;                     for (int j = 0; j < 4; ++j) r4[j] = __builtin_amdgcn_rcpf(e4[j]);
;                     const f32x4 o4 = (u4 * A8_SCALE + A8_SCALE) * (g4 * r4);
; #pragma unroll
;                     for (int j = 0; j < 4; ++j) o[4 * n + j] = o4[j]; }
;                 u32x2 w; w.x = pk4_fp8(o[0], o[1], o[2], o[3]); w.y = pk4_fp8(o[4], o[5], o[6], o[7]);
;                 *(u32x2*)(act + ro) = w; }
	v_cvt_pk_fp8_f32 v27, v30, v31
	v_fma_f32 v21, v29, 4.0, 4.0
	v_mul_f32_e32 v21, v21, v25
	v_add_u32_e32 v22, 0x90, v20
	v_cvt_pk_fp8_f32 v26, v36, v37 op_sel:[0,0,1]
	v_cvt_pk_fp8_f32 v27, v24, v21 op_sel:[0,0,1]
	v_ashrrev_i32_e32 v23, 31, v22
	v_lshlrev_b64 v[22:23], 11, v[22:23]
	v_lshl_add_u64 v[22:23], v[18:19], 0, v[22:23]
	global_store_dwordx2 v[22:23], v[26:27], off nt
	v_pk_add_f32 v[26:27], v[78:79], v[14:15]
	v_pk_add_f32 v[24:25], v[80:81], v[16:17]
	v_min_f32_e32 v26, 0x40e00000, v26
	v_min_f32_e32 v27, 0x40e00000, v27
	v_min_f32_e32 v24, 0x40e00000, v24
	v_mul_f32_e32 v21, 0xc01d265f, v26
	v_min_f32_e32 v25, 0x40e00000, v25
	v_exp_f32_e32 v32, v21
	v_mul_f32_e32 v21, 0xc01d265f, v27
	v_mul_f32_e32 v23, 0xc01d265f, v24
	v_exp_f32_e32 v34, v23
	v_mul_f32_e32 v23, 0xc01d265f, v25
	v_exp_f32_e32 v33, v21
	v_exp_f32_e32 v35, v23
	v_pk_add_f32 v[30:31], v[82:83], v[10:11]
	v_pk_add_f32 v[28:29], v[84:85], v[12:13]
	v_pk_add_f32 v[32:33], v[32:33], 1.0 op_sel_hi:[1,0]
	v_med3_f32 v21, v30, s80, v225
	v_med3_f32 v23, v31, s80, v225
	v_pk_add_f32 v[30:31], v[34:35], 1.0 op_sel_hi:[1,0]
	v_rcp_f32_e32 v32, v32
	v_rcp_f32_e32 v33, v33
	v_rcp_f32_e32 v30, v30
	v_rcp_f32_e32 v31, v31
	v_med3_f32 v28, v28, s80, v225
	v_pk_mul_f32 v[26:27], v[26:27], v[32:33]
	v_fma_f32 v21, v21, 4.0, 4.0
	v_med3_f32 v29, v29, s80, v225
	v_pk_mul_f32 v[24:25], v[24:25], v[30:31]
	v_mul_f32_e32 v21, v21, v26
	v_fma_f32 v26, v28, 4.0, 4.0
	v_fma_f32 v23, v23, 4.0, 4.0
	v_mul_f32_e32 v36, v26, v24
	v_fma_f32 v24, v29, 4.0, 4.0
	v_mul_f32_e32 v23, v23, v27
	v_mul_f32_e32 v37, v24, v25
	v_pk_add_f32 v[24:25], v[72:73], v[8:9]
	v_pk_add_f32 v[26:27], v[70:71], v[6:7]
	v_min_f32_e32 v24, 0x40e00000, v24
	v_min_f32_e32 v26, 0x40e00000, v26
	v_min_f32_e32 v27, 0x40e00000, v27
	v_min_f32_e32 v25, 0x40e00000, v25
	v_mul_f32_e32 v32, 0xc01d265f, v26
	v_mul_f32_e32 v33, 0xc01d265f, v27
	v_mul_f32_e32 v34, 0xc01d265f, v24
	v_mul_f32_e32 v35, 0xc01d265f, v25
	v_exp_f32_e32 v32, v32
	v_exp_f32_e32 v34, v34
	v_exp_f32_e32 v35, v35
	v_exp_f32_e32 v33, v33
	v_pk_add_f32 v[30:31], v[74:75], v[2:3]
	v_pk_add_f32 v[28:29], v[76:77], v[4:5]
	v_med3_f32 v38, v30, s80, v225
	v_med3_f32 v39, v31, s80, v225
	v_pk_add_f32 v[30:31], v[34:35], 1.0 op_sel_hi:[1,0]
	v_pk_add_f32 v[32:33], v[32:33], 1.0 op_sel_hi:[1,0]
	v_rcp_f32_e32 v30, v30
	v_rcp_f32_e32 v32, v32
	v_rcp_f32_e32 v31, v31
	v_rcp_f32_e32 v33, v33
	v_med3_f32 v28, v28, s80, v225
	v_med3_f32 v29, v29, s80, v225
	v_pk_mul_f32 v[24:25], v[24:25], v[30:31]
	v_pk_mul_f32 v[26:27], v[26:27], v[32:33]
	v_fma_f32 v30, v38, 4.0, 4.0
	v_mul_f32_e32 v30, v30, v26
	v_fma_f32 v26, v39, 4.0, 4.0
	v_mul_f32_e32 v31, v26, v27
	v_fma_f32 v26, v28, 4.0, 4.0
	v_mul_f32_e32 v24, v26, v24
	v_mov_b32_e32 v26, 0
	v_mov_b32_e32 v27, 0
	v_cvt_pk_fp8_f32 v26, v21, v23
	v_cvt_pk_fp8_f32 v27, v30, v31
	v_fma_f32 v21, v29, 4.0, 4.0
	v_mul_f32_e32 v21, v21, v25
	v_add_u32_e32 v22, 0xa0, v20
	v_cvt_pk_fp8_f32 v26, v36, v37 op_sel:[0,0,1]
	v_cvt_pk_fp8_f32 v27, v24, v21 op_sel:[0,0,1]
	v_ashrrev_i32_e32 v23, 31, v22
	v_lshlrev_b64 v[22:23], 11, v[22:23]
	v_pk_add_f32 v[16:17], v[64:65], v[16:17]
	v_pk_add_f32 v[14:15], v[62:63], v[14:15]
	v_lshl_add_u64 v[22:23], v[18:19], 0, v[22:23]
	v_min_f32_e32 v14, 0x40e00000, v14
	v_min_f32_e32 v16, 0x40e00000, v16
	global_store_dwordx2 v[22:23], v[26:27], off nt
	v_min_f32_e32 v15, 0x40e00000, v15
	v_min_f32_e32 v17, 0x40e00000, v17
	v_mul_f32_e32 v21, 0xc01d265f, v14
	v_mul_f32_e32 v23, 0xc01d265f, v16
	v_exp_f32_e32 v22, v21
	v_mul_f32_e32 v21, 0xc01d265f, v15
	v_exp_f32_e32 v24, v23
	v_mul_f32_e32 v23, 0xc01d265f, v17
	v_exp_f32_e32 v25, v23
	v_exp_f32_e32 v23, v21
	v_pk_add_f32 v[10:11], v[66:67], v[10:11]
	v_pk_add_f32 v[12:13], v[68:69], v[12:13]
	v_med3_f32 v21, v10, s80, v225
	v_pk_add_f32 v[22:23], v[22:23], 1.0 op_sel_hi:[1,0]
	v_med3_f32 v26, v11, s80, v225
	v_rcp_f32_e32 v22, v22
	v_rcp_f32_e32 v23, v23
	v_pk_add_f32 v[10:11], v[24:25], 1.0 op_sel_hi:[1,0]
	v_med3_f32 v24, v12, s80, v225
	v_rcp_f32_e32 v10, v10
	v_rcp_f32_e32 v11, v11
	v_med3_f32 v25, v13, s80, v225
	v_pk_mul_f32 v[12:13], v[14:15], v[22:23]
	v_fma_f32 v14, v21, 4.0, 4.0
	v_mul_f32_e32 v14, v14, v12
	v_fma_f32 v12, v26, 4.0, 4.0
	v_pk_mul_f32 v[10:11], v[16:17], v[10:11]
	v_mul_f32_e32 v15, v12, v13
	v_fma_f32 v12, v24, 4.0, 4.0
	v_pk_add_f32 v[6:7], v[58:59], v[6:7]
	v_mul_f32_e32 v16, v12, v10
	v_fma_f32 v10, v25, 4.0, 4.0
	v_min_f32_e32 v6, 0x40e00000, v6
	v_min_f32_e32 v7, 0x40e00000, v7
	v_mul_f32_e32 v17, v10, v11
	v_pk_add_f32 v[8:9], v[60:61], v[8:9]
	v_mul_f32_e32 v10, 0xc01d265f, v6
	v_mul_f32_e32 v11, 0xc01d265f, v7
	v_min_f32_e32 v8, 0x40e00000, v8
	v_min_f32_e32 v9, 0x40e00000, v9
	v_exp_f32_e32 v10, v10
	v_exp_f32_e32 v11, v11
	v_mul_f32_e32 v12, 0xc01d265f, v8
	v_mul_f32_e32 v13, 0xc01d265f, v9
	v_exp_f32_e32 v12, v12
	v_exp_f32_e32 v13, v13
	v_pk_add_f32 v[10:11], v[10:11], 1.0 op_sel_hi:[1,0]
	v_pk_add_f32 v[2:3], v[54:55], v[2:3]
	v_rcp_f32_e32 v10, v10
	v_rcp_f32_e32 v11, v11
	v_med3_f32 v21, v2, s80, v225
	v_med3_f32 v22, v3, s80, v225
	v_pk_add_f32 v[2:3], v[12:13], 1.0 op_sel_hi:[1,0]
	v_pk_add_f32 v[4:5], v[56:57], v[4:5]
	v_rcp_f32_e32 v2, v2
	v_rcp_f32_e32 v3, v3
	v_med3_f32 v12, v4, s80, v225
	v_med3_f32 v13, v5, s80, v225
	v_pk_mul_f32 v[4:5], v[6:7], v[10:11]
	v_fma_f32 v6, v21, 4.0, 4.0
	v_mul_f32_e32 v6, v6, v4
	v_fma_f32 v4, v22, 4.0, 4.0
	v_pk_mul_f32 v[2:3], v[8:9], v[2:3]
	v_mul_f32_e32 v7, v4, v5
	v_fma_f32 v4, v12, 4.0, 4.0
	v_mul_f32_e32 v2, v4, v2
	v_mov_b32_e32 v4, 0
	v_mov_b32_e32 v5, 0
	v_cvt_pk_fp8_f32 v4, v14, v15
	v_cvt_pk_fp8_f32 v5, v6, v7
	v_fma_f32 v6, v13, 4.0, 4.0
	v_mul_f32_e32 v3, v6, v3
	v_add_u32_e32 v20, 0xb0, v20
	v_cvt_pk_fp8_f32 v4, v16, v17 op_sel:[0,0,1]
	v_cvt_pk_fp8_f32 v5, v2, v3 op_sel:[0,0,1]
	v_ashrrev_i32_e32 v21, 31, v20
	v_lshlrev_b64 v[2:3], 11, v[20:21]
	v_lshl_add_u64 v[2:3], v[18:19], 0, v[2:3]
	s_and_b64 vcc, exec, s[8:9]
	s_mov_b64 s[8:9], -1
	global_store_dwordx2 v[2:3], v[4:5], off nt
	s_cbranch_vccnz .LBB0_1117
	s_and_saveexec_b64 s[8:9], s[6:7]
	s_cbranch_execz .LBB0_1145
	s_ashr_i32 s41, s40, 31
	s_lshl_b64 s[10:11], s[40:41], 14
	s_add_u32 s16, s22, s10
	s_addc_u32 s17, s23, s11
	s_lshl_b32 s10, s42, 7
	s_ashr_i32 s11, s10, 31
	s_lshl_b64 s[10:11], s[10:11], 2
	s_add_u32 s10, s16, s10
	s_addc_u32 s11, s17, s11
	s_mov_b32 s16, m0
	s_mov_b32 m0, s65
	s_nop 0
	global_load_lds_dwordx4 v221, s[10:11]
	s_mov_b32 m0, s16

; #define LAS __attribute__((address_space(3)))
; __device__ __forceinline__ unsigned pk4_fp8(float a, float b, float c, float d) { int w = 0; w = __builtin_amdgcn_cvt_pk_fp8_f32(a, b, w, false); w = __builtin_amdgcn_cvt_pk_fp8_f32(c, d, w, true); return (unsigned)w; }
;     __device__ __forceinline__ void operator()(const AccT& acc, const pg8::Unit& u, int wr, int wc, int fr, int fq, const LAS float* bl, int nai) const {
;         const int row0 = u.pm * 256 + u.hx * 128 + wr * 64 + fr, a0 = u.pn * 128 + wc * 32 + 8 * fq;
;         unsigned char* act = (unsigned char*)(ws + WS_ACT);
;         const f32x4 bg0 = *(const LAS f32x4*)(bl + 8 * fq), bg1 = *(const LAS f32x4*)(bl + 8 * fq + 4), bu0 = *(const LAS f32x4*)(bl + 32 + 8 * fq), bu1 = *(const LAS f32x4*)(bl + 32 + 8 * fq + 4);
; #pragma unroll
;         for (int ai = 0; ai < 2; ++ai) if (ai < nai)
; #pragma unroll
;             for (int m = 0; m < 4; ++m) { const size_t ro = (size_t)(row0 + ai * 128 + m * 16) * DFF + a0; float o[8];
; #pragma unroll
;                 for (int n = 0; n < 2; ++n) {
;                     f32x4 g4 = acc[ai][0][m][n] + (n ? bg1 : bg0), u4 = acc[ai][1][m][n] + (n ? bu1 : bu0);
; #pragma unroll
;                     for (int j = 0; j < 4; ++j) { g4[j] = fminf(g4[j], 7.0f); u4[j] = __builtin_amdgcn_fmed3f(u4[j], -7.0f, 7.0f); }
;                     const f32x4 t4 = g4 * (-1.702f * 1.4426950408889634f);
;                     f32x4 e4;
; #pragma unroll
;                     for (int j = 0; j < 4; ++j) e4[j] = __builtin_amdgcn_exp2f(t4[j]);
;                     e4 = e4 + 1.0f;
;                     f32x4 r4;
; #pragma unroll
;                     for (int j = 0; j < 4; ++j) r4[j] = __builtin_amdgcn_rcpf(e4[j]);
;                     const f32x4 o4 = (u4 * A8_SCALE + A8_SCALE) * (g4 * r4);
; #pragma unroll
;                     for (int j = 0; j < 4; ++j) o[4 * n + j] = o4[j]; }
;                 u32x2 w; w.x = pk4_fp8(o[0], o[1], o[2], o[3]); w.y = pk4_fp8(o[4], o[5], o[6], o[7]);
;                 *(u32x2*)(act + ro) = w; }
.LBB0_1192:
	s_nop 15
	s_nop 15
	ds_read_b128 v[14:17], v156
	ds_read_b128 v[6:9], v156 offset:16
	ds_read_b128 v[10:13], v156 offset:128
	ds_read_b128 v[2:5], v156 offset:144
	v_lshl_or_b32 v18, s44, 7, v158
	s_waitcnt lgkmcnt(3)
	v_pk_add_f32 v[22:23], v[108:109], v[16:17]
	v_pk_add_f32 v[24:25], v[106:107], v[14:15]
	v_min_f32_e32 v22, 0x40e00000, v22
	v_min_f32_e32 v24, 0x40e00000, v24
	v_min_f32_e32 v25, 0x40e00000, v25
	v_min_f32_e32 v23, 0x40e00000, v23
	v_mul_f32_e32 v21, 0xc01d265f, v24
	v_mul_f32_e32 v31, 0xc01d265f, v22
	v_exp_f32_e32 v30, v21
	v_mul_f32_e32 v21, 0xc01d265f, v25
	v_exp_f32_e32 v32, v31
	v_mul_f32_e32 v31, 0xc01d265f, v23
	v_exp_f32_e32 v33, v31
	v_exp_f32_e32 v31, v21
	s_waitcnt lgkmcnt(1)
	v_pk_add_f32 v[28:29], v[114:115], v[10:11]
	v_pk_add_f32 v[26:27], v[116:117], v[12:13]
	v_med3_f32 v21, v28, s73, v161
	v_pk_add_f32 v[30:31], v[30:31], 1.0 op_sel_hi:[1,0]
	v_med3_f32 v34, v29, s73, v161
	v_rcp_f32_e32 v30, v30
	v_rcp_f32_e32 v31, v31
	v_pk_add_f32 v[28:29], v[32:33], 1.0 op_sel_hi:[1,0]
	v_fma_f32 v21, v21, 4.0, 4.0
	v_rcp_f32_e32 v28, v28
	v_rcp_f32_e32 v29, v29
	v_pk_mul_f32 v[24:25], v[24:25], v[30:31]
	v_med3_f32 v26, v26, s73, v161
	v_mul_f32_e32 v21, v21, v24
	v_fma_f32 v24, v34, 4.0, 4.0
	v_med3_f32 v27, v27, s73, v161
	v_pk_mul_f32 v[22:23], v[22:23], v[28:29]
	v_mul_f32_e32 v34, v24, v25
	v_fma_f32 v24, v26, 4.0, 4.0
	v_mul_f32_e32 v35, v24, v22
	v_fma_f32 v22, v27, 4.0, 4.0
	v_mul_f32_e32 v36, v22, v23
	v_pk_add_f32 v[22:23], v[104:105], v[8:9]
	v_pk_add_f32 v[24:25], v[102:103], v[6:7]
	v_min_f32_e32 v22, 0x40e00000, v22
	v_min_f32_e32 v24, 0x40e00000, v24
	v_min_f32_e32 v25, 0x40e00000, v25
	v_min_f32_e32 v23, 0x40e00000, v23
	v_mul_f32_e32 v30, 0xc01d265f, v24
	v_mul_f32_e32 v31, 0xc01d265f, v25
	v_mul_f32_e32 v32, 0xc01d265f, v22
	v_mul_f32_e32 v33, 0xc01d265f, v23
	v_exp_f32_e32 v30, v30
	v_exp_f32_e32 v32, v32
	v_exp_f32_e32 v33, v33
	v_exp_f32_e32 v31, v31
	s_waitcnt lgkmcnt(0)
	v_pk_add_f32 v[28:29], v[110:111], v[2:3]
	v_pk_add_f32 v[26:27], v[112:113], v[4:5]
	v_med3_f32 v37, v28, s73, v161
	v_med3_f32 v38, v29, s73, v161
	v_pk_add_f32 v[28:29], v[32:33], 1.0 op_sel_hi:[1,0]
	v_pk_add_f32 v[30:31], v[30:31], 1.0 op_sel_hi:[1,0]
	v_rcp_f32_e32 v28, v28
	v_rcp_f32_e32 v30, v30
	v_rcp_f32_e32 v29, v29
	v_rcp_f32_e32 v31, v31
	v_med3_f32 v26, v26, s73, v161
	v_med3_f32 v27, v27, s73, v161
	v_pk_mul_f32 v[22:23], v[22:23], v[28:29]
	v_pk_mul_f32 v[24:25], v[24:25], v[30:31]
	v_fma_f32 v28, v37, 4.0, 4.0
	v_mul_f32_e32 v28, v28, v24
	v_fma_f32 v24, v38, 4.0, 4.0
	v_mul_f32_e32 v29, v24, v25
	v_fma_f32 v24, v26, 4.0, 4.0
	v_mul_f32_e32 v22, v24, v22
	v_mov_b32_e32 v24, 0
	v_mov_b32_e32 v25, 0
	v_cvt_pk_fp8_f32 v24, v21, v34
	v_cvt_pk_fp8_f32 v25, v28, v29
	v_fma_f32 v21, v27, 4.0, 4.0
	v_mul_f32_e32 v21, v21, v23
	v_lshl_add_u32 v20, s77, 8, v155
	v_cvt_pk_fp8_f32 v24, v35, v36 op_sel:[0,0,1]
	v_cvt_pk_fp8_f32 v25, v22, v21 op_sel:[0,0,1]
	v_ashrrev_i32_e32 v19, 31, v18
	v_ashrrev_i32_e32 v21, 31, v20
	v_lshl_add_u64 v[18:19], s[28:29], 0, v[18:19]
	v_lshlrev_b64 v[22:23], 11, v[20:21]
	v_lshl_add_u64 v[22:23], v[18:19], 0, v[22:23]
	v_pk_add_f32 v[26:27], v[90:91], v[14:15]
	global_store_dwordx2 v[22:23], v[24:25], off nt
	v_pk_add_f32 v[24:25], v[92:93], v[16:17]
	v_min_f32_e32 v26, 0x40e00000, v26
	v_min_f32_e32 v27, 0x40e00000, v27
	v_min_f32_e32 v24, 0x40e00000, v24
	v_mul_f32_e32 v21, 0xc01d265f, v26
	v_min_f32_e32 v25, 0x40e00000, v25
	v_exp_f32_e32 v32, v21
	v_mul_f32_e32 v21, 0xc01d265f, v27
	v_mul_f32_e32 v23, 0xc01d265f, v24
	v_exp_f32_e32 v34, v23
	v_mul_f32_e32 v23, 0xc01d265f, v25
	v_exp_f32_e32 v33, v21
	v_exp_f32_e32 v35, v23
	v_pk_add_f32 v[30:31], v[98:99], v[10:11]
	v_pk_add_f32 v[28:29], v[100:101], v[12:13]
	v_pk_add_f32 v[32:33], v[32:33], 1.0 op_sel_hi:[1,0]
	v_med3_f32 v21, v30, s73, v161
	v_med3_f32 v23, v31, s73, v161
	v_pk_add_f32 v[30:31], v[34:35], 1.0 op_sel_hi:[1,0]
	v_rcp_f32_e32 v32, v32
	v_rcp_f32_e32 v33, v33
	v_rcp_f32_e32 v30, v30
	v_rcp_f32_e32 v31, v31
	v_med3_f32 v28, v28, s73, v161
	v_pk_mul_f32 v[26:27], v[26:27], v[32:33]
	v_fma_f32 v21, v21, 4.0, 4.0
	v_med3_f32 v29, v29, s73, v161
	v_pk_mul_f32 v[24:25], v[24:25], v[30:31]
	v_mul_f32_e32 v21, v21, v26
	v_fma_f32 v26, v28, 4.0, 4.0
	v_fma_f32 v23, v23, 4.0, 4.0
	v_mul_f32_e32 v36, v26, v24
	v_fma_f32 v24, v29, 4.0, 4.0
	v_mul_f32_e32 v23, v23, v27
	v_mul_f32_e32 v37, v24, v25
	v_pk_add_f32 v[24:25], v[88:89], v[8:9]
	v_pk_add_f32 v[26:27], v[86:87], v[6:7]
	v_min_f32_e32 v24, 0x40e00000, v24
	v_min_f32_e32 v26, 0x40e00000, v26
	v_min_f32_e32 v27, 0x40e00000, v27
	v_min_f32_e32 v25, 0x40e00000, v25
	v_mul_f32_e32 v32, 0xc01d265f, v26
	v_mul_f32_e32 v33, 0xc01d265f, v27
	v_mul_f32_e32 v34, 0xc01d265f, v24
	v_mul_f32_e32 v35, 0xc01d265f, v25
	v_exp_f32_e32 v32, v32
	v_exp_f32_e32 v34, v34
	v_exp_f32_e32 v35, v35
	v_exp_f32_e32 v33, v33
	v_pk_add_f32 v[30:31], v[94:95], v[2:3]
	v_pk_add_f32 v[28:29], v[96:97], v[4:5]
	v_med3_f32 v38, v30, s73, v161
	v_med3_f32 v39, v31, s73, v161
	v_pk_add_f32 v[30:31], v[34:35], 1.0 op_sel_hi:[1,0]
	v_pk_add_f32 v[32:33], v[32:33], 1.0 op_sel_hi:[1,0]
	v_rcp_f32_e32 v30, v30
	v_rcp_f32_e32 v32, v32
	v_rcp_f32_e32 v31, v31
	v_rcp_f32_e32 v33, v33
	v_med3_f32 v28, v28, s73, v161
	v_med3_f32 v29, v29, s73, v161
	v_pk_mul_f32 v[24:25], v[24:25], v[30:31]
	v_pk_mul_f32 v[26:27], v[26:27], v[32:33]
	v_fma_f32 v30, v38, 4.0, 4.0
	v_mul_f32_e32 v30, v30, v26
	v_fma_f32 v26, v39, 4.0, 4.0
	v_mul_f32_e32 v31, v26, v27
	v_fma_f32 v26, v28, 4.0, 4.0
	v_mul_f32_e32 v24, v26, v24
	v_mov_b32_e32 v26, 0
	v_mov_b32_e32 v27, 0
	v_cvt_pk_fp8_f32 v26, v21, v23
	v_cvt_pk_fp8_f32 v27, v30, v31
; #define LAS __attribute__((address_space(3)))
; __device__ __forceinline__ unsigned pk4_fp8(float a, float b, float c, float d) { int w = 0; w = __builtin_amdgcn_cvt_pk_fp8_f32(a, b, w, false); w = __builtin_amdgcn_cvt_pk_fp8_f32(c, d, w, true); return (unsigned)w; }
;     __device__ __forceinline__ void operator()(const AccT& acc, const pg8::Unit& u, int wr, int wc, int fr, int fq, const LAS float* bl, int nai) const {
;         const int row0 = u.pm * 256 + u.hx * 128 + wr * 64 + fr, a0 = u.pn * 128 + wc * 32 + 8 * fq;
;         unsigned char* act = (unsigned char*)(ws + WS_ACT);
;         const f32x4 bg0 = *(const LAS f32x4*)(bl + 8 * fq), bg1 = *(const LAS f32x4*)(bl + 8 * fq + 4), bu0 = *(const LAS f32x4*)(bl + 32 + 8 * fq), bu1 = *(const LAS f32x4*)(bl + 32 + 8 * fq + 4);
; #pragma unroll
;         for (int ai = 0; ai < 2; ++ai) if (ai < nai)
; #pragma unroll
;             for (int m = 0; m < 4; ++m) { const size_t ro = (size_t)(row0 + ai * 128 + m * 16) * DFF + a0; float o[8];
; #pragma unroll
;                 for (int n = 0; n < 2; ++n) {
;                     f32x4 g4 = acc[ai][0][m][n] + (n ? bg1 : bg0), u4 = acc[ai][1][m][n] + (n ? bu1 : bu0);
; #pragma unroll
;                     for (int j = 0; j < 4; ++j) { g4[j] = fminf(g4[j], 7.0f); u4[j] = __builtin_amdgcn_fmed3f(u4[j], -7.0f, 7.0f); }
;                     const f32x4 t4 = g4 * (-1.702f * 1.4426950408889634f);
;                     f32x4 e4;
; #pragma unroll
;                     for (int j = 0; j < 4; ++j) e4[j] = __builtin_amdgcn_exp2f(t4[j]);
;                     e4 = e4 + 1.0f;
;                     f32x4 r4;
; #pragma unroll
;                     for (int j = 0; j < 4; ++j) r4[j] = __builtin_amdgcn_rcpf(e4[j]);
;                     const f32x4 o4 = (u4 * A8_SCALE + A8_SCALE) * (g4 * r4);
; #pragma unroll
;                     for (int j = 0; j < 4; ++j) o[4 * n + j] = o4[j]; }
;                 u32x2 w; w.x = pk4_fp8(o[0], o[1], o[2], o[3]); w.y = pk4_fp8(o[4], o[5], o[6], o[7]);
;                 *(u32x2*)(act + ro) = w; }
	v_fma_f32 v21, v29, 4.0, 4.0
	v_mul_f32_e32 v21, v21, v25
	v_or_b32_e32 v22, 16, v20
	v_cvt_pk_fp8_f32 v26, v36, v37 op_sel:[0,0,1]
	v_cvt_pk_fp8_f32 v27, v24, v21 op_sel:[0,0,1]
	v_ashrrev_i32_e32 v23, 31, v22
	v_lshlrev_b64 v[22:23], 11, v[22:23]
	v_lshl_add_u64 v[22:23], v[18:19], 0, v[22:23]
	global_store_dwordx2 v[22:23], v[26:27], off nt
	v_pk_add_f32 v[26:27], v[78:79], v[14:15]
	v_pk_add_f32 v[24:25], v[80:81], v[16:17]
	v_min_f32_e32 v26, 0x40e00000, v26
	v_min_f32_e32 v27, 0x40e00000, v27
	v_min_f32_e32 v24, 0x40e00000, v24
	v_mul_f32_e32 v21, 0xc01d265f, v26
	v_min_f32_e32 v25, 0x40e00000, v25
	v_exp_f32_e32 v32, v21
	v_mul_f32_e32 v21, 0xc01d265f, v27
	v_mul_f32_e32 v23, 0xc01d265f, v24
	v_exp_f32_e32 v34, v23
	v_mul_f32_e32 v23, 0xc01d265f, v25
	v_exp_f32_e32 v33, v21
	v_exp_f32_e32 v35, v23
	v_pk_add_f32 v[30:31], v[82:83], v[10:11]
	v_pk_add_f32 v[28:29], v[84:85], v[12:13]
	v_pk_add_f32 v[32:33], v[32:33], 1.0 op_sel_hi:[1,0]
	v_med3_f32 v21, v30, s73, v161
	v_med3_f32 v23, v31, s73, v161
	v_pk_add_f32 v[30:31], v[34:35], 1.0 op_sel_hi:[1,0]
	v_rcp_f32_e32 v32, v32
	v_rcp_f32_e32 v33, v33
	v_rcp_f32_e32 v30, v30
	v_rcp_f32_e32 v31, v31
	v_med3_f32 v28, v28, s73, v161
	v_pk_mul_f32 v[26:27], v[26:27], v[32:33]
	v_fma_f32 v21, v21, 4.0, 4.0
	v_med3_f32 v29, v29, s73, v161
	v_pk_mul_f32 v[24:25], v[24:25], v[30:31]
	v_mul_f32_e32 v21, v21, v26
	v_fma_f32 v26, v28, 4.0, 4.0
	v_fma_f32 v23, v23, 4.0, 4.0
	v_mul_f32_e32 v36, v26, v24
	v_fma_f32 v24, v29, 4.0, 4.0
	v_mul_f32_e32 v23, v23, v27
	v_mul_f32_e32 v37, v24, v25
	v_pk_add_f32 v[24:25], v[72:73], v[8:9]
	v_pk_add_f32 v[26:27], v[70:71], v[6:7]
	v_min_f32_e32 v24, 0x40e00000, v24
	v_min_f32_e32 v26, 0x40e00000, v26
	v_min_f32_e32 v27, 0x40e00000, v27
	v_min_f32_e32 v25, 0x40e00000, v25
	v_mul_f32_e32 v32, 0xc01d265f, v26
	v_mul_f32_e32 v33, 0xc01d265f, v27
	v_mul_f32_e32 v34, 0xc01d265f, v24
	v_mul_f32_e32 v35, 0xc01d265f, v25
	v_exp_f32_e32 v32, v32
	v_exp_f32_e32 v34, v34
	v_exp_f32_e32 v35, v35
	v_exp_f32_e32 v33, v33
	v_pk_add_f32 v[30:31], v[74:75], v[2:3]
	v_pk_add_f32 v[28:29], v[76:77], v[4:5]
	v_med3_f32 v38, v30, s73, v161
	v_med3_f32 v39, v31, s73, v161
	v_pk_add_f32 v[30:31], v[34:35], 1.0 op_sel_hi:[1,0]
	v_pk_add_f32 v[32:33], v[32:33], 1.0 op_sel_hi:[1,0]
	v_rcp_f32_e32 v30, v30
	v_rcp_f32_e32 v32, v32
	v_rcp_f32_e32 v31, v31
	v_rcp_f32_e32 v33, v33
	v_med3_f32 v28, v28, s73, v161
	v_med3_f32 v29, v29, s73, v161
	v_pk_mul_f32 v[24:25], v[24:25], v[30:31]
	v_pk_mul_f32 v[26:27], v[26:27], v[32:33]
	v_fma_f32 v30, v38, 4.0, 4.0
	v_mul_f32_e32 v30, v30, v26
	v_fma_f32 v26, v39, 4.0, 4.0
	v_mul_f32_e32 v31, v26, v27
	v_fma_f32 v26, v28, 4.0, 4.0
	v_mul_f32_e32 v24, v26, v24
	v_mov_b32_e32 v26, 0
	v_mov_b32_e32 v27, 0
	v_cvt_pk_fp8_f32 v26, v21, v23
	v_cvt_pk_fp8_f32 v27, v30, v31
	v_fma_f32 v21, v29, 4.0, 4.0
	v_mul_f32_e32 v21, v21, v25
	v_or_b32_e32 v22, 32, v20
	v_cvt_pk_fp8_f32 v26, v36, v37 op_sel:[0,0,1]
	v_cvt_pk_fp8_f32 v27, v24, v21 op_sel:[0,0,1]
	v_ashrrev_i32_e32 v23, 31, v22
	v_lshlrev_b64 v[22:23], 11, v[22:23]
	v_pk_add_f32 v[16:17], v[64:65], v[16:17]
	v_pk_add_f32 v[14:15], v[62:63], v[14:15]
	v_lshl_add_u64 v[22:23], v[18:19], 0, v[22:23]
	v_min_f32_e32 v14, 0x40e00000, v14
	v_min_f32_e32 v16, 0x40e00000, v16
	global_store_dwordx2 v[22:23], v[26:27], off nt
	v_min_f32_e32 v15, 0x40e00000, v15
	v_min_f32_e32 v17, 0x40e00000, v17
	v_mul_f32_e32 v21, 0xc01d265f, v14
	v_mul_f32_e32 v23, 0xc01d265f, v16
	v_exp_f32_e32 v22, v21
	v_mul_f32_e32 v21, 0xc01d265f, v15
	v_exp_f32_e32 v24, v23
	v_mul_f32_e32 v23, 0xc01d265f, v17
	v_exp_f32_e32 v25, v23
	v_exp_f32_e32 v23, v21
	v_pk_add_f32 v[10:11], v[66:67], v[10:11]
	v_pk_add_f32 v[12:13], v[68:69], v[12:13]
	v_med3_f32 v21, v10, s73, v161
	v_pk_add_f32 v[22:23], v[22:23], 1.0 op_sel_hi:[1,0]
	v_med3_f32 v26, v11, s73, v161
	v_rcp_f32_e32 v22, v22
	v_rcp_f32_e32 v23, v23
	v_pk_add_f32 v[10:11], v[24:25], 1.0 op_sel_hi:[1,0]
	v_med3_f32 v24, v12, s73, v161
	v_rcp_f32_e32 v10, v10
	v_rcp_f32_e32 v11, v11
	v_med3_f32 v25, v13, s73, v161
	v_pk_mul_f32 v[12:13], v[14:15], v[22:23]
	v_fma_f32 v14, v21, 4.0, 4.0
	v_mul_f32_e32 v14, v14, v12
	v_fma_f32 v12, v26, 4.0, 4.0
	v_pk_mul_f32 v[10:11], v[16:17], v[10:11]
	v_mul_f32_e32 v15, v12, v13
	v_fma_f32 v12, v24, 4.0, 4.0
	v_pk_add_f32 v[6:7], v[58:59], v[6:7]
	v_mul_f32_e32 v16, v12, v10
	v_fma_f32 v10, v25, 4.0, 4.0
	v_min_f32_e32 v6, 0x40e00000, v6
	v_min_f32_e32 v7, 0x40e00000, v7
	v_mul_f32_e32 v17, v10, v11
	v_pk_add_f32 v[8:9], v[60:61], v[8:9]
	v_mul_f32_e32 v10, 0xc01d265f, v6
	v_mul_f32_e32 v11, 0xc01d265f, v7
	v_min_f32_e32 v8, 0x40e00000, v8
	v_min_f32_e32 v9, 0x40e00000, v9
	v_exp_f32_e32 v10, v10
	v_exp_f32_e32 v11, v11
	v_mul_f32_e32 v12, 0xc01d265f, v8
	v_mul_f32_e32 v13, 0xc01d265f, v9
	v_exp_f32_e32 v12, v12
	v_exp_f32_e32 v13, v13
	v_pk_add_f32 v[10:11], v[10:11], 1.0 op_sel_hi:[1,0]
	v_pk_add_f32 v[2:3], v[54:55], v[2:3]
	v_rcp_f32_e32 v10, v10
	v_rcp_f32_e32 v11, v11
	v_med3_f32 v21, v2, s73, v161
	v_med3_f32 v22, v3, s73, v161
	v_pk_add_f32 v[2:3], v[12:13], 1.0 op_sel_hi:[1,0]
	v_pk_add_f32 v[4:5], v[56:57], v[4:5]
	v_rcp_f32_e32 v2, v2
	v_rcp_f32_e32 v3, v3
	v_med3_f32 v12, v4, s73, v161
	v_med3_f32 v13, v5, s73, v161
	v_pk_mul_f32 v[4:5], v[6:7], v[10:11]
	v_fma_f32 v6, v21, 4.0, 4.0
	v_mul_f32_e32 v6, v6, v4
	v_fma_f32 v4, v22, 4.0, 4.0
	v_pk_mul_f32 v[2:3], v[8:9], v[2:3]
	v_mul_f32_e32 v7, v4, v5
	v_fma_f32 v4, v12, 4.0, 4.0
	v_mul_f32_e32 v2, v4, v2
	v_mov_b32_e32 v4, 0
	v_mov_b32_e32 v5, 0
	v_cvt_pk_fp8_f32 v4, v14, v15
	v_cvt_pk_fp8_f32 v5, v6, v7
	v_fma_f32 v6, v13, 4.0, 4.0
	v_mul_f32_e32 v3, v6, v3
	v_or_b32_e32 v20, 48, v20
	v_cvt_pk_fp8_f32 v4, v16, v17 op_sel:[0,0,1]
	v_cvt_pk_fp8_f32 v5, v2, v3 op_sel:[0,0,1]
	v_ashrrev_i32_e32 v21, 31, v20
	v_lshlrev_b64 v[2:3], 11, v[20:21]
	v_lshl_add_u64 v[2:3], v[18:19], 0, v[2:3]
	s_and_b64 vcc, exec, s[8:9]
	s_mov_b64 s[8:9], -1
	global_store_dwordx2 v[2:3], v[4:5], off nt
	s_cbranch_vccnz .LBB0_1165
	s_and_saveexec_b64 s[8:9], s[6:7]
	s_cbranch_execz .LBB0_1195
	s_ashr_i32 s39, s38, 31
	s_lshl_b64 s[10:11], s[38:39], 14
	s_add_u32 s39, s22, s10
	s_addc_u32 s41, s23, s11
	s_lshl_b32 s10, s40, 7
	s_ashr_i32 s11, s10, 31
	s_lshl_b64 s[10:11], s[10:11], 2
	s_add_u32 s10, s39, s10
	s_addc_u32 s11, s41, s11
	s_mov_b32 s39, m0
	s_mov_b32 m0, s59
	s_nop 0
	global_load_lds_dwordx4 v157, s[10:11]
	s_mov_b32 m0, s39

; #define LAS __attribute__((address_space(3)))
; __device__ __forceinline__ unsigned pk4_fp8(float a, float b, float c, float d) { int w = 0; w = __builtin_amdgcn_cvt_pk_fp8_f32(a, b, w, false); w = __builtin_amdgcn_cvt_pk_fp8_f32(c, d, w, true); return (unsigned)w; }
;     __device__ __forceinline__ void operator()(const AccT& acc, const pg8::Unit& u, int wr, int wc, int fr, int fq, const LAS float* bl, const LAS int* rid, int nai) const {
;         const int col0 = u.pn * 256 + wc * 64 + 16 * fq;
;         unsigned char* y = (unsigned char*)(ws + WS_Y);
;         const int nvalid = __builtin_amdgcn_readfirstlane(cnt[u.e]) - u.mt * 256;
;         f32x4 bv[2][2];
; #pragma unroll
;         for (int bj = 0; bj < 2; ++bj) { bv[bj][0] = *(const LAS f32x4*)(bl + 16 * fq + 8 * bj) * Y8_SCALE; bv[bj][1] = *(const LAS f32x4*)(bl + 16 * fq + 8 * bj + 4) * Y8_SCALE; }
; #pragma unroll
;         for (int ai = 0; ai < 2; ++ai) if (ai < nai)
; #pragma unroll
;             for (int m = 0; m < 4; ++m) { const int rl = u.hx * 128 + ai * 128 + wr * 64 + m * 16 + fr; const int dst = rid[ai * 64 + m * 16 + fr];
;                 if (rl < nvalid) { const size_t ro = (size_t)dst * D + col0; unsigned wv[4];
; #pragma unroll
;                     for (int bj = 0; bj < 2; ++bj) { const f32x4 v0 = acc[ai][bj][m][0] * Y8_SCALE + bv[bj][0], v1 = acc[ai][bj][m][1] * Y8_SCALE + bv[bj][1];
;                         wv[2 * bj] = pk4_fp8(v0[0], v0[1], v0[2], v0[3]); wv[2 * bj + 1] = pk4_fp8(v1[0], v1[1], v1[2], v1[3]); }
;                     *(u32x4*)(y + ro) = (u32x4){wv[0], wv[1], wv[2], wv[3]}; } }
.LBB0_1302:
	v_pk_fma_f32 v[22:23], v[158:159], s[22:23], v[18:19] op_sel_hi:[1,0,1]
	v_pk_fma_f32 v[26:27], v[154:155], s[22:23], v[16:17] op_sel_hi:[1,0,1]
	v_mov_b32_e32 v20, 0
	v_mov_b32_e32 v21, 0
	v_cvt_pk_fp8_f32 v20, v22, v23
	v_cvt_pk_fp8_f32 v21, v26, v27
	v_pk_fma_f32 v[22:23], v[160:161], s[22:23], v[8:9] op_sel_hi:[1,0,1]
	v_pk_fma_f32 v[26:27], v[156:157], s[22:23], v[14:15] op_sel_hi:[1,0,1]
	v_cvt_pk_fp8_f32 v20, v22, v23 op_sel:[0,0,1]
	v_cvt_pk_fp8_f32 v21, v26, v27 op_sel:[0,0,1]
	v_pk_fma_f32 v[26:27], v[150:151], s[22:23], v[12:13] op_sel_hi:[1,0,1]
	v_pk_fma_f32 v[28:29], v[146:147], s[22:23], v[10:11] op_sel_hi:[1,0,1]
	v_mov_b32_e32 v22, 0
	v_mov_b32_e32 v23, 0
	ds_read_b32 v24, v173
	v_cvt_pk_fp8_f32 v22, v26, v27
	v_cvt_pk_fp8_f32 v23, v28, v29
	v_pk_fma_f32 v[26:27], v[152:153], s[22:23], v[2:3] op_sel_hi:[1,0,1]
	v_pk_fma_f32 v[28:29], v[148:149], s[22:23], v[6:7] op_sel_hi:[1,0,1]
	v_cvt_pk_fp8_f32 v22, v26, v27 op_sel:[0,0,1]
	v_cvt_pk_fp8_f32 v23, v28, v29 op_sel:[0,0,1]
	s_waitcnt lgkmcnt(0)
	v_ashrrev_i32_e32 v25, 31, v24
	v_lshlrev_b64 v[24:25], 11, v[24:25]
	v_lshl_add_u64 v[24:25], v[4:5], 0, v[24:25]
	global_store_dwordx4 v[24:25], v[20:23], off nt
	s_or_b64 exec, exec, s[34:35]
	v_cmp_gt_i32_e32 vcc, s25, v174
	s_and_saveexec_b64 s[34:35], vcc
	s_cbranch_execz .LBB0_1295
.LBB0_1303:
	v_pk_fma_f32 v[22:23], v[142:143], s[22:23], v[18:19] op_sel_hi:[1,0,1]
	v_pk_fma_f32 v[26:27], v[138:139], s[22:23], v[16:17] op_sel_hi:[1,0,1]
	v_mov_b32_e32 v20, 0
	v_mov_b32_e32 v21, 0
	v_cvt_pk_fp8_f32 v20, v22, v23
	v_cvt_pk_fp8_f32 v21, v26, v27
	v_pk_fma_f32 v[22:23], v[144:145], s[22:23], v[8:9] op_sel_hi:[1,0,1]
	v_pk_fma_f32 v[26:27], v[140:141], s[22:23], v[14:15] op_sel_hi:[1,0,1]
	v_cvt_pk_fp8_f32 v20, v22, v23 op_sel:[0,0,1]
	v_cvt_pk_fp8_f32 v21, v26, v27 op_sel:[0,0,1]
	v_pk_fma_f32 v[26:27], v[134:135], s[22:23], v[12:13] op_sel_hi:[1,0,1]
	v_pk_fma_f32 v[28:29], v[130:131], s[22:23], v[10:11] op_sel_hi:[1,0,1]
	v_mov_b32_e32 v22, 0
	v_mov_b32_e32 v23, 0
	ds_read_b32 v24, v173 offset:64
	v_cvt_pk_fp8_f32 v22, v26, v27
	v_cvt_pk_fp8_f32 v23, v28, v29
	v_pk_fma_f32 v[26:27], v[136:137], s[22:23], v[2:3] op_sel_hi:[1,0,1]
	v_pk_fma_f32 v[28:29], v[132:133], s[22:23], v[6:7] op_sel_hi:[1,0,1]
	v_cvt_pk_fp8_f32 v22, v26, v27 op_sel:[0,0,1]
	v_cvt_pk_fp8_f32 v23, v28, v29 op_sel:[0,0,1]
	s_waitcnt lgkmcnt(0)
	v_ashrrev_i32_e32 v25, 31, v24
	v_lshlrev_b64 v[24:25], 11, v[24:25]
	v_lshl_add_u64 v[24:25], v[4:5], 0, v[24:25]
	global_store_dwordx4 v[24:25], v[20:23], off nt
	s_or_b64 exec, exec, s[34:35]
	v_cmp_gt_i32_e32 vcc, s25, v175
	s_and_saveexec_b64 s[34:35], vcc
	s_cbranch_execz .LBB0_1296
.LBB0_1304:
	v_pk_fma_f32 v[22:23], v[126:127], s[22:23], v[18:19] op_sel_hi:[1,0,1]
	v_pk_fma_f32 v[26:27], v[122:123], s[22:23], v[16:17] op_sel_hi:[1,0,1]
	v_mov_b32_e32 v20, 0
	v_mov_b32_e32 v21, 0
	v_cvt_pk_fp8_f32 v20, v22, v23
	v_cvt_pk_fp8_f32 v21, v26, v27
	v_pk_fma_f32 v[22:23], v[128:129], s[22:23], v[8:9] op_sel_hi:[1,0,1]
	v_pk_fma_f32 v[26:27], v[124:125], s[22:23], v[14:15] op_sel_hi:[1,0,1]
	v_cvt_pk_fp8_f32 v20, v22, v23 op_sel:[0,0,1]
	v_cvt_pk_fp8_f32 v21, v26, v27 op_sel:[0,0,1]
	v_pk_fma_f32 v[26:27], v[118:119], s[22:23], v[12:13] op_sel_hi:[1,0,1]
	v_pk_fma_f32 v[28:29], v[114:115], s[22:23], v[10:11] op_sel_hi:[1,0,1]
	v_mov_b32_e32 v22, 0
	v_mov_b32_e32 v23, 0
	ds_read_b32 v24, v173 offset:128
	v_cvt_pk_fp8_f32 v22, v26, v27
	v_cvt_pk_fp8_f32 v23, v28, v29
	v_pk_fma_f32 v[26:27], v[120:121], s[22:23], v[2:3] op_sel_hi:[1,0,1]
	v_pk_fma_f32 v[28:29], v[116:117], s[22:23], v[6:7] op_sel_hi:[1,0,1]
	v_cvt_pk_fp8_f32 v22, v26, v27 op_sel:[0,0,1]
	v_cvt_pk_fp8_f32 v23, v28, v29 op_sel:[0,0,1]
	s_waitcnt lgkmcnt(0)
	v_ashrrev_i32_e32 v25, 31, v24
	v_lshlrev_b64 v[24:25], 11, v[24:25]
	v_lshl_add_u64 v[24:25], v[4:5], 0, v[24:25]
	global_store_dwordx4 v[24:25], v[20:23], off nt
	s_or_b64 exec, exec, s[34:35]
	v_cmp_gt_i32_e32 vcc, s25, v176
	s_and_saveexec_b64 s[34:35], vcc
	s_cbranch_execz .LBB0_1297
.LBB0_1305:
	v_pk_fma_f32 v[22:23], v[110:111], s[22:23], v[18:19] op_sel_hi:[1,0,1]
	v_pk_fma_f32 v[26:27], v[106:107], s[22:23], v[16:17] op_sel_hi:[1,0,1]
	v_mov_b32_e32 v20, 0
	v_mov_b32_e32 v21, 0
	v_cvt_pk_fp8_f32 v20, v22, v23
	v_cvt_pk_fp8_f32 v21, v26, v27
	v_pk_fma_f32 v[22:23], v[112:113], s[22:23], v[8:9] op_sel_hi:[1,0,1]
	v_pk_fma_f32 v[26:27], v[108:109], s[22:23], v[14:15] op_sel_hi:[1,0,1]
	v_cvt_pk_fp8_f32 v20, v22, v23 op_sel:[0,0,1]
	v_cvt_pk_fp8_f32 v21, v26, v27 op_sel:[0,0,1]
	v_pk_fma_f32 v[26:27], v[102:103], s[22:23], v[12:13] op_sel_hi:[1,0,1]
	v_pk_fma_f32 v[28:29], v[98:99], s[22:23], v[10:11] op_sel_hi:[1,0,1]
	v_mov_b32_e32 v22, 0
	v_mov_b32_e32 v23, 0
	ds_read_b32 v24, v173 offset:192
	v_cvt_pk_fp8_f32 v22, v26, v27
	v_cvt_pk_fp8_f32 v23, v28, v29
	v_pk_fma_f32 v[26:27], v[104:105], s[22:23], v[2:3] op_sel_hi:[1,0,1]
	v_pk_fma_f32 v[28:29], v[100:101], s[22:23], v[6:7] op_sel_hi:[1,0,1]
	v_cvt_pk_fp8_f32 v22, v26, v27 op_sel:[0,0,1]
	v_cvt_pk_fp8_f32 v23, v28, v29 op_sel:[0,0,1]
	s_waitcnt lgkmcnt(0)
	v_ashrrev_i32_e32 v25, 31, v24
	v_lshlrev_b64 v[24:25], 11, v[24:25]
	v_lshl_add_u64 v[24:25], v[4:5], 0, v[24:25]
	global_store_dwordx4 v[24:25], v[20:23], off nt
	s_or_b64 exec, exec, s[34:35]
	v_cmp_gt_i32_e32 vcc, s25, v177
	s_and_saveexec_b64 s[34:35], vcc
	s_cbranch_execz .LBB0_1298
; #define LAS __attribute__((address_space(3)))
; __device__ __forceinline__ unsigned pk4_fp8(float a, float b, float c, float d) { int w = 0; w = __builtin_amdgcn_cvt_pk_fp8_f32(a, b, w, false); w = __builtin_amdgcn_cvt_pk_fp8_f32(c, d, w, true); return (unsigned)w; }
;     __device__ __forceinline__ void operator()(const AccT& acc, const pg8::Unit& u, int wr, int wc, int fr, int fq, const LAS float* bl, const LAS int* rid, int nai) const {
;         const int col0 = u.pn * 256 + wc * 64 + 16 * fq;
;         unsigned char* y = (unsigned char*)(ws + WS_Y);
;         const int nvalid = __builtin_amdgcn_readfirstlane(cnt[u.e]) - u.mt * 256;
;         f32x4 bv[2][2];
; #pragma unroll
;         for (int bj = 0; bj < 2; ++bj) { bv[bj][0] = *(const LAS f32x4*)(bl + 16 * fq + 8 * bj) * Y8_SCALE; bv[bj][1] = *(const LAS f32x4*)(bl + 16 * fq + 8 * bj + 4) * Y8_SCALE; }
; #pragma unroll
;         for (int ai = 0; ai < 2; ++ai) if (ai < nai)
; #pragma unroll
;             for (int m = 0; m < 4; ++m) { const int rl = u.hx * 128 + ai * 128 + wr * 64 + m * 16 + fr; const int dst = rid[ai * 64 + m * 16 + fr];
;                 if (rl < nvalid) { const size_t ro = (size_t)dst * D + col0; unsigned wv[4];
; #pragma unroll
;                     for (int bj = 0; bj < 2; ++bj) { const f32x4 v0 = acc[ai][bj][m][0] * Y8_SCALE + bv[bj][0], v1 = acc[ai][bj][m][1] * Y8_SCALE + bv[bj][1];
;                         wv[2 * bj] = pk4_fp8(v0[0], v0[1], v0[2], v0[3]); wv[2 * bj + 1] = pk4_fp8(v1[0], v1[1], v1[2], v1[3]); }
;                     *(u32x4*)(y + ro) = (u32x4){wv[0], wv[1], wv[2], wv[3]}; } }
.LBB0_1306:
	v_pk_fma_f32 v[22:23], v[94:95], s[22:23], v[18:19] op_sel_hi:[1,0,1]
	v_pk_fma_f32 v[26:27], v[90:91], s[22:23], v[16:17] op_sel_hi:[1,0,1]
	v_mov_b32_e32 v20, 0
	v_mov_b32_e32 v21, 0
	v_cvt_pk_fp8_f32 v20, v22, v23
	v_cvt_pk_fp8_f32 v21, v26, v27
	v_pk_fma_f32 v[22:23], v[96:97], s[22:23], v[8:9] op_sel_hi:[1,0,1]
	v_pk_fma_f32 v[26:27], v[92:93], s[22:23], v[14:15] op_sel_hi:[1,0,1]
	v_cvt_pk_fp8_f32 v20, v22, v23 op_sel:[0,0,1]
	v_cvt_pk_fp8_f32 v21, v26, v27 op_sel:[0,0,1]
	v_pk_fma_f32 v[26:27], v[86:87], s[22:23], v[12:13] op_sel_hi:[1,0,1]
	v_pk_fma_f32 v[28:29], v[82:83], s[22:23], v[10:11] op_sel_hi:[1,0,1]
	v_mov_b32_e32 v22, 0
	v_mov_b32_e32 v23, 0
	ds_read_b32 v24, v173 offset:256
	v_cvt_pk_fp8_f32 v22, v26, v27
	v_cvt_pk_fp8_f32 v23, v28, v29
	v_pk_fma_f32 v[26:27], v[88:89], s[22:23], v[2:3] op_sel_hi:[1,0,1]
	v_pk_fma_f32 v[28:29], v[84:85], s[22:23], v[6:7] op_sel_hi:[1,0,1]
	v_cvt_pk_fp8_f32 v22, v26, v27 op_sel:[0,0,1]
	v_cvt_pk_fp8_f32 v23, v28, v29 op_sel:[0,0,1]
	s_waitcnt lgkmcnt(0)
	v_ashrrev_i32_e32 v25, 31, v24
	v_lshlrev_b64 v[24:25], 11, v[24:25]
	v_lshl_add_u64 v[24:25], v[4:5], 0, v[24:25]
	global_store_dwordx4 v[24:25], v[20:23], off nt
	s_or_b64 exec, exec, s[34:35]
	v_cmp_gt_i32_e32 vcc, s25, v178
	s_and_saveexec_b64 s[34:35], vcc
	s_cbranch_execz .LBB0_1299
.LBB0_1307:
	v_pk_fma_f32 v[22:23], v[78:79], s[22:23], v[18:19] op_sel_hi:[1,0,1]
	v_pk_fma_f32 v[26:27], v[74:75], s[22:23], v[16:17] op_sel_hi:[1,0,1]
	v_mov_b32_e32 v20, 0
	v_mov_b32_e32 v21, 0
	v_cvt_pk_fp8_f32 v20, v22, v23
	v_cvt_pk_fp8_f32 v21, v26, v27
	v_pk_fma_f32 v[22:23], v[80:81], s[22:23], v[8:9] op_sel_hi:[1,0,1]
	v_pk_fma_f32 v[26:27], v[76:77], s[22:23], v[14:15] op_sel_hi:[1,0,1]
	v_cvt_pk_fp8_f32 v20, v22, v23 op_sel:[0,0,1]
	v_cvt_pk_fp8_f32 v21, v26, v27 op_sel:[0,0,1]
	v_pk_fma_f32 v[26:27], v[70:71], s[22:23], v[12:13] op_sel_hi:[1,0,1]
	v_pk_fma_f32 v[28:29], v[66:67], s[22:23], v[10:11] op_sel_hi:[1,0,1]
	v_mov_b32_e32 v22, 0
	v_mov_b32_e32 v23, 0
	ds_read_b32 v24, v173 offset:320
	v_cvt_pk_fp8_f32 v22, v26, v27
	v_cvt_pk_fp8_f32 v23, v28, v29
	v_pk_fma_f32 v[26:27], v[72:73], s[22:23], v[2:3] op_sel_hi:[1,0,1]
	v_pk_fma_f32 v[28:29], v[68:69], s[22:23], v[6:7] op_sel_hi:[1,0,1]
	v_cvt_pk_fp8_f32 v22, v26, v27 op_sel:[0,0,1]
	v_cvt_pk_fp8_f32 v23, v28, v29 op_sel:[0,0,1]
	s_waitcnt lgkmcnt(0)
	v_ashrrev_i32_e32 v25, 31, v24
	v_lshlrev_b64 v[24:25], 11, v[24:25]
	v_lshl_add_u64 v[24:25], v[4:5], 0, v[24:25]
	global_store_dwordx4 v[24:25], v[20:23], off nt
	s_or_b64 exec, exec, s[34:35]
	v_cmp_gt_i32_e32 vcc, s25, v179
	s_and_saveexec_b64 s[34:35], vcc
	s_cbranch_execz .LBB0_1300
.LBB0_1308:
	v_pk_fma_f32 v[22:23], v[62:63], s[22:23], v[18:19] op_sel_hi:[1,0,1]
	v_pk_fma_f32 v[26:27], v[58:59], s[22:23], v[16:17] op_sel_hi:[1,0,1]
	v_mov_b32_e32 v20, 0
	v_mov_b32_e32 v21, 0
	v_cvt_pk_fp8_f32 v20, v22, v23
	v_cvt_pk_fp8_f32 v21, v26, v27
	v_pk_fma_f32 v[22:23], v[64:65], s[22:23], v[8:9] op_sel_hi:[1,0,1]
	v_pk_fma_f32 v[26:27], v[60:61], s[22:23], v[14:15] op_sel_hi:[1,0,1]
	v_cvt_pk_fp8_f32 v20, v22, v23 op_sel:[0,0,1]
	v_cvt_pk_fp8_f32 v21, v26, v27 op_sel:[0,0,1]
	v_pk_fma_f32 v[26:27], v[54:55], s[22:23], v[12:13] op_sel_hi:[1,0,1]
	v_pk_fma_f32 v[28:29], v[50:51], s[22:23], v[10:11] op_sel_hi:[1,0,1]
	v_mov_b32_e32 v22, 0
	v_mov_b32_e32 v23, 0
	ds_read_b32 v24, v173 offset:384
	v_cvt_pk_fp8_f32 v22, v26, v27
	v_cvt_pk_fp8_f32 v23, v28, v29
	v_pk_fma_f32 v[26:27], v[56:57], s[22:23], v[2:3] op_sel_hi:[1,0,1]
	v_pk_fma_f32 v[28:29], v[52:53], s[22:23], v[6:7] op_sel_hi:[1,0,1]
	v_cvt_pk_fp8_f32 v22, v26, v27 op_sel:[0,0,1]
	v_cvt_pk_fp8_f32 v23, v28, v29 op_sel:[0,0,1]
	s_waitcnt lgkmcnt(0)
	v_ashrrev_i32_e32 v25, 31, v24
	v_lshlrev_b64 v[24:25], 11, v[24:25]
	v_lshl_add_u64 v[24:25], v[4:5], 0, v[24:25]
	global_store_dwordx4 v[24:25], v[20:23], off nt
	s_or_b64 exec, exec, s[34:35]
	v_cmp_gt_i32_e32 vcc, s25, v180
	s_and_saveexec_b64 s[34:35], vcc
	s_cbranch_execz .LBB0_1301
.LBB0_1309:
	v_pk_fma_f32 v[18:19], v[46:47], s[22:23], v[18:19] op_sel_hi:[1,0,1]
	v_pk_fma_f32 v[22:23], v[42:43], s[22:23], v[16:17] op_sel_hi:[1,0,1]
	v_mov_b32_e32 v16, 0
	v_cvt_pk_fp8_f32 v16, v18, v19
	v_pk_fma_f32 v[8:9], v[48:49], s[22:23], v[8:9] op_sel_hi:[1,0,1]
	v_mov_b32_e32 v17, 0
	v_pk_fma_f32 v[10:11], v[34:35], s[22:23], v[10:11] op_sel_hi:[1,0,1]
	v_cvt_pk_fp8_f32 v16, v8, v9 op_sel:[0,0,1]
	v_pk_fma_f32 v[8:9], v[38:39], s[22:23], v[12:13] op_sel_hi:[1,0,1]
	v_mov_b32_e32 v18, 0
	v_mov_b32_e32 v19, 0
	ds_read_b32 v20, v173 offset:448
	v_cvt_pk_fp8_f32 v17, v22, v23
	v_cvt_pk_fp8_f32 v18, v8, v9
	v_cvt_pk_fp8_f32 v19, v10, v11
	v_pk_fma_f32 v[14:15], v[44:45], s[22:23], v[14:15] op_sel_hi:[1,0,1]
	v_pk_fma_f32 v[2:3], v[40:41], s[22:23], v[2:3] op_sel_hi:[1,0,1]
	v_pk_fma_f32 v[6:7], v[36:37], s[22:23], v[6:7] op_sel_hi:[1,0,1]
	v_cvt_pk_fp8_f32 v17, v14, v15 op_sel:[0,0,1]
	v_cvt_pk_fp8_f32 v18, v2, v3 op_sel:[0,0,1]
	v_cvt_pk_fp8_f32 v19, v6, v7 op_sel:[0,0,1]
	s_waitcnt lgkmcnt(0)
	v_ashrrev_i32_e32 v21, 31, v20
	v_lshlrev_b64 v[2:3], 11, v[20:21]
	v_lshl_add_u64 v[2:3], v[4:5], 0, v[2:3]
	global_store_dwordx4 v[2:3], v[16:19], off nt
	s_or_b64 exec, exec, s[34:35]
	s_and_b64 vcc, exec, s[10:11]
	s_mov_b64 s[10:11], -1
	s_cbranch_vccnz .LBB0_1280

; #define LAS __attribute__((address_space(3)))
; __device__ __forceinline__ unsigned pk4_fp8(float a, float b, float c, float d) { int w = 0; w = __builtin_amdgcn_cvt_pk_fp8_f32(a, b, w, false); w = __builtin_amdgcn_cvt_pk_fp8_f32(c, d, w, true); return (unsigned)w; }
;     __device__ __forceinline__ void operator()(const AccT& acc, const pg8::Unit& u, int wr, int wc, int fr, int fq, const LAS float* bl, const LAS int* rid, int nai) const {
;         const int col0 = u.pn * 256 + wc * 64 + 16 * fq;
;         unsigned char* y = (unsigned char*)(ws + WS_Y);
;         const int nvalid = __builtin_amdgcn_readfirstlane(cnt[u.e]) - u.mt * 256;
;         f32x4 bv[2][2];
; #pragma unroll
;         for (int bj = 0; bj < 2; ++bj) { bv[bj][0] = *(const LAS f32x4*)(bl + 16 * fq + 8 * bj) * Y8_SCALE; bv[bj][1] = *(const LAS f32x4*)(bl + 16 * fq + 8 * bj + 4) * Y8_SCALE; }
; #pragma unroll
;         for (int ai = 0; ai < 2; ++ai) if (ai < nai)
; #pragma unroll
;             for (int m = 0; m < 4; ++m) { const int rl = u.hx * 128 + ai * 128 + wr * 64 + m * 16 + fr; const int dst = rid[ai * 64 + m * 16 + fr];
;                 if (rl < nvalid) { const size_t ro = (size_t)dst * D + col0; unsigned wv[4];
; #pragma unroll
;                     for (int bj = 0; bj < 2; ++bj) { const f32x4 v0 = acc[ai][bj][m][0] * Y8_SCALE + bv[bj][0], v1 = acc[ai][bj][m][1] * Y8_SCALE + bv[bj][1];
;                         wv[2 * bj] = pk4_fp8(v0[0], v0[1], v0[2], v0[3]); wv[2 * bj + 1] = pk4_fp8(v1[0], v1[1], v1[2], v1[3]); }
;                     *(u32x4*)(y + ro) = (u32x4){wv[0], wv[1], wv[2], wv[3]}; } }
.LBB0_1354:
	v_pk_fma_f32 v[108:109], v[58:59], s[22:23], v[82:83] op_sel_hi:[1,0,1]
	v_mov_b32_e32 v59, 0
	v_cvt_pk_fp8_f32 v59, v108, v109
	v_pk_fma_f32 v[60:61], v[60:61], s[22:23], v[80:81] op_sel_hi:[1,0,1]
	v_pk_fma_f32 v[62:63], v[62:63], s[22:23], v[84:85] op_sel_hi:[1,0,1]
	v_mov_b32_e32 v58, 0
	v_cvt_pk_fp8_f32 v59, v60, v61 op_sel:[0,0,1]
	v_pk_fma_f32 v[54:55], v[54:55], s[22:23], v[78:79] op_sel_hi:[1,0,1]
	v_pk_fma_f32 v[50:51], v[50:51], s[22:23], v[76:77] op_sel_hi:[1,0,1]
	v_mov_b32_e32 v60, 0
	v_mov_b32_e32 v61, 0
	ds_read_b32 v106, v93
	v_cvt_pk_fp8_f32 v58, v62, v63
	v_cvt_pk_fp8_f32 v60, v54, v55
	v_cvt_pk_fp8_f32 v61, v50, v51
	v_pk_fma_f32 v[62:63], v[64:65], s[22:23], v[74:75] op_sel_hi:[1,0,1]
	v_pk_fma_f32 v[50:51], v[56:57], s[22:23], v[68:69] op_sel_hi:[1,0,1]
	v_pk_fma_f32 v[52:53], v[52:53], s[22:23], v[72:73] op_sel_hi:[1,0,1]
	v_cvt_pk_fp8_f32 v58, v62, v63 op_sel:[0,0,1]
	v_cvt_pk_fp8_f32 v60, v50, v51 op_sel:[0,0,1]
	v_cvt_pk_fp8_f32 v61, v52, v53 op_sel:[0,0,1]
	s_waitcnt lgkmcnt(0)
	v_ashrrev_i32_e32 v107, 31, v106
	v_lshlrev_b64 v[50:51], 11, v[106:107]
	v_lshl_add_u64 v[50:51], v[70:71], 0, v[50:51]
	global_store_dwordx4 v[50:51], v[58:61], off nt
	s_or_b64 exec, exec, s[26:27]
	v_cmp_gt_i32_e32 vcc, s25, v94
	s_and_saveexec_b64 s[26:27], vcc
	s_cbranch_execz .LBB0_1351
.LBB0_1355:
	v_pk_fma_f32 v[52:53], v[42:43], s[22:23], v[82:83] op_sel_hi:[1,0,1]
	v_mov_b32_e32 v43, 0
	v_cvt_pk_fp8_f32 v43, v52, v53
	v_pk_fma_f32 v[44:45], v[44:45], s[22:23], v[80:81] op_sel_hi:[1,0,1]
	v_pk_fma_f32 v[46:47], v[46:47], s[22:23], v[84:85] op_sel_hi:[1,0,1]
	v_mov_b32_e32 v42, 0
	v_cvt_pk_fp8_f32 v43, v44, v45 op_sel:[0,0,1]
	v_pk_fma_f32 v[38:39], v[38:39], s[22:23], v[78:79] op_sel_hi:[1,0,1]
	v_pk_fma_f32 v[34:35], v[34:35], s[22:23], v[76:77] op_sel_hi:[1,0,1]
	v_mov_b32_e32 v44, 0
	v_mov_b32_e32 v45, 0
	ds_read_b32 v50, v93 offset:64
	v_cvt_pk_fp8_f32 v42, v46, v47
	v_cvt_pk_fp8_f32 v44, v38, v39
	v_cvt_pk_fp8_f32 v45, v34, v35
	v_pk_fma_f32 v[46:47], v[48:49], s[22:23], v[74:75] op_sel_hi:[1,0,1]
	v_pk_fma_f32 v[34:35], v[40:41], s[22:23], v[68:69] op_sel_hi:[1,0,1]
	v_pk_fma_f32 v[36:37], v[36:37], s[22:23], v[72:73] op_sel_hi:[1,0,1]
	v_cvt_pk_fp8_f32 v42, v46, v47 op_sel:[0,0,1]
	v_cvt_pk_fp8_f32 v44, v34, v35 op_sel:[0,0,1]
	v_cvt_pk_fp8_f32 v45, v36, v37 op_sel:[0,0,1]
	s_waitcnt lgkmcnt(0)
	v_ashrrev_i32_e32 v51, 31, v50
	v_lshlrev_b64 v[34:35], 11, v[50:51]
	v_lshl_add_u64 v[34:35], v[70:71], 0, v[34:35]
	global_store_dwordx4 v[34:35], v[42:45], off nt
	s_or_b64 exec, exec, s[26:27]
	v_cmp_gt_i32_e32 vcc, s25, v95
	s_and_saveexec_b64 s[26:27], vcc
	s_cbranch_execz .LBB0_1352
.LBB0_1356:
	v_pk_fma_f32 v[36:37], v[26:27], s[22:23], v[82:83] op_sel_hi:[1,0,1]
	v_mov_b32_e32 v27, 0
	v_cvt_pk_fp8_f32 v27, v36, v37
	v_pk_fma_f32 v[28:29], v[28:29], s[22:23], v[80:81] op_sel_hi:[1,0,1]
	v_pk_fma_f32 v[30:31], v[30:31], s[22:23], v[84:85] op_sel_hi:[1,0,1]
	v_mov_b32_e32 v26, 0
	v_cvt_pk_fp8_f32 v27, v28, v29 op_sel:[0,0,1]
	v_pk_fma_f32 v[22:23], v[22:23], s[22:23], v[78:79] op_sel_hi:[1,0,1]
	v_pk_fma_f32 v[18:19], v[18:19], s[22:23], v[76:77] op_sel_hi:[1,0,1]
	v_mov_b32_e32 v28, 0
	v_mov_b32_e32 v29, 0
	ds_read_b32 v34, v93 offset:128
	v_cvt_pk_fp8_f32 v26, v30, v31
	v_cvt_pk_fp8_f32 v28, v22, v23
	v_cvt_pk_fp8_f32 v29, v18, v19
	v_pk_fma_f32 v[30:31], v[32:33], s[22:23], v[74:75] op_sel_hi:[1,0,1]
	v_pk_fma_f32 v[18:19], v[24:25], s[22:23], v[68:69] op_sel_hi:[1,0,1]
	v_pk_fma_f32 v[20:21], v[20:21], s[22:23], v[72:73] op_sel_hi:[1,0,1]
	v_cvt_pk_fp8_f32 v26, v30, v31 op_sel:[0,0,1]
	v_cvt_pk_fp8_f32 v28, v18, v19 op_sel:[0,0,1]
	v_cvt_pk_fp8_f32 v29, v20, v21 op_sel:[0,0,1]
	s_waitcnt lgkmcnt(0)
	v_ashrrev_i32_e32 v35, 31, v34
	v_lshlrev_b64 v[18:19], 11, v[34:35]
	v_lshl_add_u64 v[18:19], v[70:71], 0, v[18:19]
	global_store_dwordx4 v[18:19], v[26:29], off nt
	s_or_b64 exec, exec, s[26:27]
	v_cmp_gt_i32_e32 vcc, s25, v96
	s_and_saveexec_b64 s[26:27], vcc
	s_cbranch_execz .LBB0_1353
.LBB0_1357:
	v_pk_fma_f32 v[20:21], v[10:11], s[22:23], v[82:83] op_sel_hi:[1,0,1]
	v_mov_b32_e32 v11, 0
	v_cvt_pk_fp8_f32 v11, v20, v21
	v_pk_fma_f32 v[12:13], v[12:13], s[22:23], v[80:81] op_sel_hi:[1,0,1]
	v_pk_fma_f32 v[14:15], v[14:15], s[22:23], v[84:85] op_sel_hi:[1,0,1]
	v_mov_b32_e32 v10, 0
	v_cvt_pk_fp8_f32 v11, v12, v13 op_sel:[0,0,1]
	v_pk_fma_f32 v[6:7], v[6:7], s[22:23], v[78:79] op_sel_hi:[1,0,1]
	v_pk_fma_f32 v[2:3], v[2:3], s[22:23], v[76:77] op_sel_hi:[1,0,1]
	v_mov_b32_e32 v12, 0
	v_mov_b32_e32 v13, 0
	ds_read_b32 v18, v93 offset:192
	v_cvt_pk_fp8_f32 v10, v14, v15
	v_cvt_pk_fp8_f32 v12, v6, v7
	v_cvt_pk_fp8_f32 v13, v2, v3
	v_pk_fma_f32 v[14:15], v[16:17], s[22:23], v[74:75] op_sel_hi:[1,0,1]
	v_pk_fma_f32 v[2:3], v[8:9], s[22:23], v[68:69] op_sel_hi:[1,0,1]
	v_pk_fma_f32 v[4:5], v[4:5], s[22:23], v[72:73] op_sel_hi:[1,0,1]
	v_cvt_pk_fp8_f32 v10, v14, v15 op_sel:[0,0,1]
	v_cvt_pk_fp8_f32 v12, v2, v3 op_sel:[0,0,1]
	v_cvt_pk_fp8_f32 v13, v4, v5 op_sel:[0,0,1]
	s_waitcnt lgkmcnt(0)
	v_ashrrev_i32_e32 v19, 31, v18
	v_lshlrev_b64 v[2:3], 11, v[18:19]
	v_lshl_add_u64 v[2:3], v[70:71], 0, v[2:3]
	global_store_dwordx4 v[2:3], v[10:13], off nt
	s_or_b64 exec, exec, s[26:27]
	s_and_b64 vcc, exec, s[10:11]
	s_mov_b64 s[10:11], -1
	s_cbranch_vccnz .LBB0_1334
